# speedup vs baseline: 1.0925x; 1.0925x over previous
.LBB0_47:
	s_andn2_b64 vcc, exec, s[4:5]
	s_cbranch_vccnz .LBB0_54
	s_add_i32 s3, s2, 0xfffffe00
	s_load_dwordx2 s[6:7], s[0:1], 0x28
	s_load_dwordx2 s[4:5], s[0:1], 0x58
	s_lshr_b32 s3, s3, 3
	s_bfe_u32 s11, s2, 0x10002
	s_lshl_b32 s8, s3, 7
	s_lshl_b32 s9, s11, 6
	s_or_b32 s8, s9, s8
	s_and_b32 s10, s2, 3
	s_mul_hi_u32 s9, s8, 0x640
	s_mulk_i32 s8, 0x640
	s_mulk_i32 s10, 0x64
	s_waitcnt lgkmcnt(0)
	s_add_u32 s6, s6, s8
	s_addc_u32 s7, s7, s9
	s_lshl_b32 s8, s10, 2
	s_add_u32 s8, s6, s8
	s_addc_u32 s9, s7, 0
	s_movk_i32 s12, 0x4b0
	s_mov_b32 s13, 0xffffc7c2
	s_mov_b32 s14, 0x43000000
	v_lshrrev_b16_e32 v2, 2, v0
	v_mul_u32_u24_e32 v2, 0x147b, v2
	v_lshrrev_b32_e32 v2, 17, v2
	v_lshlrev_b32_e32 v3, 2, v0
	v_mad_u32_u24 v3, v2, s12, v3
	global_load_dword v8, v3, s[8:9] nt
	v_mul_u32_u24_e32 v4, 0x90, v0
	v_mad_i32_i24 v33, v2, s13, v4
	v_add_u32_e32 v1, 0x100, v0
	v_lshrrev_b16_e32 v2, 2, v1
	v_mul_u32_u24_e32 v2, 0x147b, v2
	v_lshrrev_b32_e32 v2, 17, v2
	v_lshlrev_b32_e32 v3, 2, v1
	v_mad_u32_u24 v3, v2, s12, v3
	global_load_dword v9, v3, s[8:9] nt
	v_mul_u32_u24_e32 v4, 0x90, v1
	v_mad_i32_i24 v34, v2, s13, v4
	v_add_u32_e32 v1, 0x200, v0
	v_lshrrev_b16_e32 v2, 2, v1
	v_mul_u32_u24_e32 v2, 0x147b, v2
	v_lshrrev_b32_e32 v2, 17, v2
	v_lshlrev_b32_e32 v3, 2, v1
	v_mad_u32_u24 v3, v2, s12, v3
	global_load_dword v10, v3, s[8:9] nt
	v_mul_u32_u24_e32 v4, 0x90, v1
	v_mad_i32_i24 v35, v2, s13, v4
	v_add_u32_e32 v1, 0x300, v0
	v_lshrrev_b16_e32 v2, 2, v1
	v_mul_u32_u24_e32 v2, 0x147b, v2
	v_lshrrev_b32_e32 v2, 17, v2
	v_lshlrev_b32_e32 v3, 2, v1
	v_mad_u32_u24 v3, v2, s12, v3
	global_load_dword v11, v3, s[8:9] nt
	v_mul_u32_u24_e32 v4, 0x90, v1
	v_mad_i32_i24 v36, v2, s13, v4
	v_add_u32_e32 v1, 0x400, v0
	v_lshrrev_b16_e32 v2, 2, v1
	v_mul_u32_u24_e32 v2, 0x147b, v2
	v_lshrrev_b32_e32 v2, 17, v2
	v_lshlrev_b32_e32 v3, 2, v1
	v_mad_u32_u24 v3, v2, s12, v3
	global_load_dword v12, v3, s[8:9] nt
	v_mul_u32_u24_e32 v4, 0x90, v1
	v_mad_i32_i24 v37, v2, s13, v4
	v_add_u32_e32 v1, 0x500, v0
	v_lshrrev_b16_e32 v2, 2, v1
	v_mul_u32_u24_e32 v2, 0x147b, v2
	v_lshrrev_b32_e32 v2, 17, v2
	v_lshlrev_b32_e32 v3, 2, v1
	v_mad_u32_u24 v3, v2, s12, v3
	global_load_dword v13, v3, s[8:9] nt
	v_mul_u32_u24_e32 v4, 0x90, v1
	v_mad_i32_i24 v38, v2, s13, v4
	v_add_u32_e32 v1, 0x600, v0
	v_lshrrev_b16_e32 v2, 2, v1
	v_mul_u32_u24_e32 v2, 0x147b, v2
	v_lshrrev_b32_e32 v2, 17, v2
	v_lshlrev_b32_e32 v3, 2, v1
	v_mad_u32_u24 v3, v2, s12, v3
	global_load_dword v14, v3, s[8:9] nt
	v_mul_u32_u24_e32 v4, 0x90, v1
	v_mad_i32_i24 v39, v2, s13, v4
	v_add_u32_e32 v1, 0x700, v0
	v_lshrrev_b16_e32 v2, 2, v1
	v_mul_u32_u24_e32 v2, 0x147b, v2
	v_lshrrev_b32_e32 v2, 17, v2
	v_lshlrev_b32_e32 v3, 2, v1
	v_mad_u32_u24 v3, v2, s12, v3
	global_load_dword v15, v3, s[8:9] nt
	v_mul_u32_u24_e32 v4, 0x90, v1
	v_mad_i32_i24 v40, v2, s13, v4
	v_add_u32_e32 v1, 0x800, v0
	v_lshrrev_b16_e32 v2, 2, v1
	v_mul_u32_u24_e32 v2, 0x147b, v2
	v_lshrrev_b32_e32 v2, 17, v2
	v_lshlrev_b32_e32 v3, 2, v1
	v_mad_u32_u24 v3, v2, s12, v3
	global_load_dword v16, v3, s[8:9] nt
	v_mul_u32_u24_e32 v4, 0x90, v1
	v_mad_i32_i24 v41, v2, s13, v4
	v_add_u32_e32 v1, 0x900, v0
	v_lshrrev_b16_e32 v2, 2, v1
	v_mul_u32_u24_e32 v2, 0x147b, v2
	v_lshrrev_b32_e32 v2, 17, v2
	v_lshlrev_b32_e32 v3, 2, v1
	v_mad_u32_u24 v3, v2, s12, v3
	global_load_dword v17, v3, s[8:9] nt
	v_mul_u32_u24_e32 v4, 0x90, v1
	v_mad_i32_i24 v42, v2, s13, v4
	v_add_u32_e32 v1, 0xa00, v0
	v_lshrrev_b16_e32 v2, 2, v1
	v_mul_u32_u24_e32 v2, 0x147b, v2
	v_lshrrev_b32_e32 v2, 17, v2
	v_lshlrev_b32_e32 v3, 2, v1
	v_mad_u32_u24 v3, v2, s12, v3
	global_load_dword v18, v3, s[8:9] nt
	v_mul_u32_u24_e32 v4, 0x90, v1
	v_mad_i32_i24 v43, v2, s13, v4
	v_add_u32_e32 v1, 0xb00, v0
	v_lshrrev_b16_e32 v2, 2, v1
	v_mul_u32_u24_e32 v2, 0x147b, v2
	v_lshrrev_b32_e32 v2, 17, v2
	v_lshlrev_b32_e32 v3, 2, v1
	v_mad_u32_u24 v3, v2, s12, v3
	global_load_dword v19, v3, s[8:9] nt
	v_mul_u32_u24_e32 v4, 0x90, v1
	v_mad_i32_i24 v44, v2, s13, v4
	v_add_u32_e32 v1, 0xc00, v0
	v_lshrrev_b16_e32 v2, 2, v1
	v_mul_u32_u24_e32 v2, 0x147b, v2
	v_lshrrev_b32_e32 v2, 17, v2
	v_lshlrev_b32_e32 v3, 2, v1
	v_mad_u32_u24 v3, v2, s12, v3
	global_load_dword v20, v3, s[8:9] nt
	v_mul_u32_u24_e32 v4, 0x90, v1
	v_mad_i32_i24 v45, v2, s13, v4
	v_add_u32_e32 v1, 0xd00, v0
	v_lshrrev_b16_e32 v2, 2, v1
	v_mul_u32_u24_e32 v2, 0x147b, v2
	v_lshrrev_b32_e32 v2, 17, v2
	v_lshlrev_b32_e32 v3, 2, v1
	v_mad_u32_u24 v3, v2, s12, v3
	global_load_dword v21, v3, s[8:9] nt
	v_mul_u32_u24_e32 v4, 0x90, v1
	v_mad_i32_i24 v46, v2, s13, v4
	v_add_u32_e32 v1, 0xe00, v0
	v_lshrrev_b16_e32 v2, 2, v1
	v_mul_u32_u24_e32 v2, 0x147b, v2
	v_lshrrev_b32_e32 v2, 17, v2
	v_lshlrev_b32_e32 v3, 2, v1
	v_mad_u32_u24 v3, v2, s12, v3
	global_load_dword v22, v3, s[8:9] nt
	v_mul_u32_u24_e32 v4, 0x90, v1
	v_mad_i32_i24 v47, v2, s13, v4
	v_add_u32_e32 v1, 0xf00, v0
	v_lshrrev_b16_e32 v2, 2, v1
	v_mul_u32_u24_e32 v2, 0x147b, v2
	v_lshrrev_b32_e32 v2, 17, v2
	v_lshlrev_b32_e32 v3, 2, v1
	v_mad_u32_u24 v3, v2, s12, v3
	global_load_dword v23, v3, s[8:9] nt
	v_mul_u32_u24_e32 v4, 0x90, v1
	v_mad_i32_i24 v48, v2, s13, v4
	v_add_u32_e32 v1, 0x1000, v0
	v_lshrrev_b16_e32 v2, 2, v1
	v_mul_u32_u24_e32 v2, 0x147b, v2
	v_lshrrev_b32_e32 v2, 17, v2
	v_lshlrev_b32_e32 v3, 2, v1
	v_mad_u32_u24 v3, v2, s12, v3
	global_load_dword v24, v3, s[8:9] nt
	v_mul_u32_u24_e32 v4, 0x90, v1
	v_mad_i32_i24 v49, v2, s13, v4
	v_add_u32_e32 v1, 0x1100, v0
	v_lshrrev_b16_e32 v2, 2, v1
	v_mul_u32_u24_e32 v2, 0x147b, v2
	v_lshrrev_b32_e32 v2, 17, v2
	v_lshlrev_b32_e32 v3, 2, v1
	v_mad_u32_u24 v3, v2, s12, v3
	global_load_dword v25, v3, s[8:9] nt
	v_mul_u32_u24_e32 v4, 0x90, v1
	v_mad_i32_i24 v50, v2, s13, v4
	v_add_u32_e32 v1, 0x1200, v0
	v_lshrrev_b16_e32 v2, 2, v1
	v_mul_u32_u24_e32 v2, 0x147b, v2
	v_lshrrev_b32_e32 v2, 17, v2
	v_lshlrev_b32_e32 v3, 2, v1
	v_mad_u32_u24 v3, v2, s12, v3
	global_load_dword v26, v3, s[8:9] nt
	v_mul_u32_u24_e32 v4, 0x90, v1
	v_mad_i32_i24 v51, v2, s13, v4
	v_add_u32_e32 v1, 0x1300, v0
	v_lshrrev_b16_e32 v2, 2, v1
	v_mul_u32_u24_e32 v2, 0x147b, v2
	v_lshrrev_b32_e32 v2, 17, v2
	v_lshlrev_b32_e32 v3, 2, v1
	v_mad_u32_u24 v3, v2, s12, v3
	global_load_dword v27, v3, s[8:9] nt
	v_mul_u32_u24_e32 v4, 0x90, v1
	v_mad_i32_i24 v52, v2, s13, v4
	v_add_u32_e32 v1, 0x1400, v0
	v_lshrrev_b16_e32 v2, 2, v1
	v_mul_u32_u24_e32 v2, 0x147b, v2
	v_lshrrev_b32_e32 v2, 17, v2
	v_lshlrev_b32_e32 v3, 2, v1
	v_mad_u32_u24 v3, v2, s12, v3
	global_load_dword v28, v3, s[8:9] nt
	v_mul_u32_u24_e32 v4, 0x90, v1
	v_mad_i32_i24 v53, v2, s13, v4
	v_add_u32_e32 v1, 0x1500, v0
	v_lshrrev_b16_e32 v2, 2, v1
	v_mul_u32_u24_e32 v2, 0x147b, v2
	v_lshrrev_b32_e32 v2, 17, v2
	v_lshlrev_b32_e32 v3, 2, v1
	v_mad_u32_u24 v3, v2, s12, v3
	global_load_dword v29, v3, s[8:9] nt
	v_mul_u32_u24_e32 v4, 0x90, v1
	v_mad_i32_i24 v54, v2, s13, v4
	v_add_u32_e32 v1, 0x1600, v0
	v_lshrrev_b16_e32 v2, 2, v1
	v_mul_u32_u24_e32 v2, 0x147b, v2
	v_lshrrev_b32_e32 v2, 17, v2
	v_lshlrev_b32_e32 v3, 2, v1
	v_mad_u32_u24 v3, v2, s12, v3
	global_load_dword v30, v3, s[8:9] nt
	v_mul_u32_u24_e32 v4, 0x90, v1
	v_mad_i32_i24 v55, v2, s13, v4
	v_add_u32_e32 v1, 0x1700, v0
	v_lshrrev_b16_e32 v2, 2, v1
	v_mul_u32_u24_e32 v2, 0x147b, v2
	v_lshrrev_b32_e32 v2, 17, v2
	v_lshlrev_b32_e32 v3, 2, v1
	v_mad_u32_u24 v3, v2, s12, v3
	global_load_dword v31, v3, s[8:9] nt
	v_mul_u32_u24_e32 v4, 0x90, v1
	v_mad_i32_i24 v56, v2, s13, v4
	v_add_u32_e32 v1, 0x1800, v0
	v_lshrrev_b16_e32 v2, 2, v1
	v_mul_u32_u24_e32 v2, 0x147b, v2
	v_lshrrev_b32_e32 v2, 17, v2
	v_lshlrev_b32_e32 v3, 2, v1
	v_mad_u32_u24 v3, v2, s12, v3
	global_load_dword v32, v3, s[8:9] nt
	v_mul_u32_u24_e32 v4, 0x90, v1
	v_mad_i32_i24 v57, v2, s13, v4
	s_waitcnt vmcnt(24)
	v_fma_mixlo_f16 v1, v8, s14, 0
	ds_write_b16 v33, v1
	s_waitcnt vmcnt(23)
	v_fma_mixlo_f16 v2, v9, s14, 0
	ds_write_b16 v34, v2
	s_waitcnt vmcnt(22)
	v_fma_mixlo_f16 v3, v10, s14, 0
	ds_write_b16 v35, v3
	s_waitcnt vmcnt(21)
	v_fma_mixlo_f16 v4, v11, s14, 0
	ds_write_b16 v36, v4
	s_waitcnt vmcnt(20)
	v_fma_mixlo_f16 v1, v12, s14, 0
	ds_write_b16 v37, v1
	s_waitcnt vmcnt(19)
	v_fma_mixlo_f16 v2, v13, s14, 0
	ds_write_b16 v38, v2
	s_waitcnt vmcnt(18)
	v_fma_mixlo_f16 v3, v14, s14, 0
	ds_write_b16 v39, v3
	s_waitcnt vmcnt(17)
	v_fma_mixlo_f16 v4, v15, s14, 0
	ds_write_b16 v40, v4
	s_waitcnt vmcnt(16)
	v_fma_mixlo_f16 v1, v16, s14, 0
	ds_write_b16 v41, v1
	s_waitcnt vmcnt(15)
	v_fma_mixlo_f16 v2, v17, s14, 0
	ds_write_b16 v42, v2
	s_waitcnt vmcnt(14)
	v_fma_mixlo_f16 v3, v18, s14, 0
	ds_write_b16 v43, v3
	s_waitcnt vmcnt(13)
	v_fma_mixlo_f16 v4, v19, s14, 0
	ds_write_b16 v44, v4
	s_waitcnt vmcnt(12)
	v_fma_mixlo_f16 v1, v20, s14, 0
	ds_write_b16 v45, v1
	s_waitcnt vmcnt(11)
	v_fma_mixlo_f16 v2, v21, s14, 0
	ds_write_b16 v46, v2
	s_waitcnt vmcnt(10)
	v_fma_mixlo_f16 v3, v22, s14, 0
	ds_write_b16 v47, v3
	s_waitcnt vmcnt(9)
	v_fma_mixlo_f16 v4, v23, s14, 0
	ds_write_b16 v48, v4
	s_waitcnt vmcnt(8)
	v_fma_mixlo_f16 v1, v24, s14, 0
	ds_write_b16 v49, v1
	s_waitcnt vmcnt(7)
	v_fma_mixlo_f16 v2, v25, s14, 0
	ds_write_b16 v50, v2
	s_waitcnt vmcnt(6)
	v_fma_mixlo_f16 v3, v26, s14, 0
	ds_write_b16 v51, v3
	s_waitcnt vmcnt(5)
	v_fma_mixlo_f16 v4, v27, s14, 0
	ds_write_b16 v52, v4
	s_waitcnt vmcnt(4)
	v_fma_mixlo_f16 v1, v28, s14, 0
	ds_write_b16 v53, v1
	s_waitcnt vmcnt(3)
	v_fma_mixlo_f16 v2, v29, s14, 0
	ds_write_b16 v54, v2
	s_waitcnt vmcnt(2)
	v_fma_mixlo_f16 v3, v30, s14, 0
	ds_write_b16 v55, v3
	s_waitcnt vmcnt(1)
	v_fma_mixlo_f16 v4, v31, s14, 0
	ds_write_b16 v56, v4
	s_waitcnt vmcnt(0)
	v_fma_mixlo_f16 v1, v32, s14, 0
	ds_write_b16 v57, v1
	s_movk_i32 s6, 0x320
	v_cmp_gt_u32_e32 vcc, s6, v0
	s_waitcnt lgkmcnt(0)
	s_barrier
	s_and_saveexec_b64 s[6:7], vcc
	s_cbranch_execz .LBB0_53
	s_mulk_i32 s11, 0x190
	v_lshrrev_b32_e32 v4, 3, v0
	s_add_i32 s10, s10, s11
	v_add_u32_e32 v2, s10, v4
	v_lshl_add_u32 v2, v2, 6, s3
	v_mov_b32_e32 v3, 0
	v_and_b32_e32 v5, 7, v0
	v_lshlrev_b64 v[2:3], 7, v[2:3]
	v_lshlrev_b32_e32 v5, 4, v5
	v_or_b32_e32 v2, v2, v5
	s_movk_i32 s3, 0x90
	v_or_b32_e32 v1, 0xffffff00, v0
	v_lshl_add_u64 v[2:3], s[4:5], 0, v[2:3]
	v_mad_u32_u24 v4, v4, s3, v5
	s_mov_b64 s[4:5], 0
	s_mov_b64 s[8:9], 0x40000
	s_movk_i32 s3, 0x21f

.LBB0_55:
	s_andn2_b64 vcc, exec, s[4:5]
	s_cbranch_vccnz .LBB0_61
	s_load_dwordx2 s[10:11], s[0:1], 0x0
	s_load_dwordx2 s[4:5], s[0:1], 0x30
	s_ashr_i32 s6, s2, 2
	s_and_b32 s7, s2, 3
	s_lshl_b32 s0, s6, 6
	s_mul_i32 s1, s6, 0x19000
	s_mul_hi_i32 s0, s0, 0x640
	s_waitcnt lgkmcnt(0)
	s_add_u32 s1, s10, s1
	s_addc_u32 s0, s11, s0
	s_mul_i32 s2, s7, 0x190
	s_add_u32 s2, s1, s2
	s_addc_u32 s3, s0, 0
	s_movk_i32 s8, 0x4b0
	s_mov_b32 s9, 0xffffc7c2
	s_mov_b32 s10, 0x43000000
	v_lshrrev_b16_e32 v2, 2, v0
	v_mul_u32_u24_e32 v2, 0x147b, v2
	v_lshrrev_b32_e32 v2, 17, v2
	v_lshlrev_b32_e32 v3, 2, v0
	v_mad_u32_u24 v3, v2, s8, v3
	global_load_dword v8, v3, s[2:3] nt
	v_mul_u32_u24_e32 v4, 0x90, v0
	v_mad_i32_i24 v33, v2, s9, v4
	v_add_u32_e32 v1, 0x100, v0
	v_lshrrev_b16_e32 v2, 2, v1
	v_mul_u32_u24_e32 v2, 0x147b, v2
	v_lshrrev_b32_e32 v2, 17, v2
	v_lshlrev_b32_e32 v3, 2, v1
	v_mad_u32_u24 v3, v2, s8, v3
	global_load_dword v9, v3, s[2:3] nt
	v_mul_u32_u24_e32 v4, 0x90, v1
	v_mad_i32_i24 v34, v2, s9, v4
	v_add_u32_e32 v1, 0x200, v0
	v_lshrrev_b16_e32 v2, 2, v1
	v_mul_u32_u24_e32 v2, 0x147b, v2
	v_lshrrev_b32_e32 v2, 17, v2
	v_lshlrev_b32_e32 v3, 2, v1
	v_mad_u32_u24 v3, v2, s8, v3
	global_load_dword v10, v3, s[2:3] nt
	v_mul_u32_u24_e32 v4, 0x90, v1
	v_mad_i32_i24 v35, v2, s9, v4
	v_add_u32_e32 v1, 0x300, v0
	v_lshrrev_b16_e32 v2, 2, v1
	v_mul_u32_u24_e32 v2, 0x147b, v2
	v_lshrrev_b32_e32 v2, 17, v2
	v_lshlrev_b32_e32 v3, 2, v1
	v_mad_u32_u24 v3, v2, s8, v3
	global_load_dword v11, v3, s[2:3] nt
	v_mul_u32_u24_e32 v4, 0x90, v1
	v_mad_i32_i24 v36, v2, s9, v4
	v_add_u32_e32 v1, 0x400, v0
	v_lshrrev_b16_e32 v2, 2, v1
	v_mul_u32_u24_e32 v2, 0x147b, v2
	v_lshrrev_b32_e32 v2, 17, v2
	v_lshlrev_b32_e32 v3, 2, v1
	v_mad_u32_u24 v3, v2, s8, v3
	global_load_dword v12, v3, s[2:3] nt
	v_mul_u32_u24_e32 v4, 0x90, v1
	v_mad_i32_i24 v37, v2, s9, v4
	v_add_u32_e32 v1, 0x500, v0
	v_lshrrev_b16_e32 v2, 2, v1
	v_mul_u32_u24_e32 v2, 0x147b, v2
	v_lshrrev_b32_e32 v2, 17, v2
	v_lshlrev_b32_e32 v3, 2, v1
	v_mad_u32_u24 v3, v2, s8, v3
	global_load_dword v13, v3, s[2:3] nt
	v_mul_u32_u24_e32 v4, 0x90, v1
	v_mad_i32_i24 v38, v2, s9, v4
	v_add_u32_e32 v1, 0x600, v0
	v_lshrrev_b16_e32 v2, 2, v1
	v_mul_u32_u24_e32 v2, 0x147b, v2
	v_lshrrev_b32_e32 v2, 17, v2
	v_lshlrev_b32_e32 v3, 2, v1
	v_mad_u32_u24 v3, v2, s8, v3
	global_load_dword v14, v3, s[2:3] nt
	v_mul_u32_u24_e32 v4, 0x90, v1
	v_mad_i32_i24 v39, v2, s9, v4
	v_add_u32_e32 v1, 0x700, v0
	v_lshrrev_b16_e32 v2, 2, v1
	v_mul_u32_u24_e32 v2, 0x147b, v2
	v_lshrrev_b32_e32 v2, 17, v2
	v_lshlrev_b32_e32 v3, 2, v1
	v_mad_u32_u24 v3, v2, s8, v3
	global_load_dword v15, v3, s[2:3] nt
	v_mul_u32_u24_e32 v4, 0x90, v1
	v_mad_i32_i24 v40, v2, s9, v4
	v_add_u32_e32 v1, 0x800, v0
	v_lshrrev_b16_e32 v2, 2, v1
	v_mul_u32_u24_e32 v2, 0x147b, v2
	v_lshrrev_b32_e32 v2, 17, v2
	v_lshlrev_b32_e32 v3, 2, v1
	v_mad_u32_u24 v3, v2, s8, v3
	global_load_dword v16, v3, s[2:3] nt
	v_mul_u32_u24_e32 v4, 0x90, v1
	v_mad_i32_i24 v41, v2, s9, v4
	v_add_u32_e32 v1, 0x900, v0
	v_lshrrev_b16_e32 v2, 2, v1
	v_mul_u32_u24_e32 v2, 0x147b, v2
	v_lshrrev_b32_e32 v2, 17, v2
	v_lshlrev_b32_e32 v3, 2, v1
	v_mad_u32_u24 v3, v2, s8, v3
	global_load_dword v17, v3, s[2:3] nt
	v_mul_u32_u24_e32 v4, 0x90, v1
	v_mad_i32_i24 v42, v2, s9, v4
	v_add_u32_e32 v1, 0xa00, v0
	v_lshrrev_b16_e32 v2, 2, v1
	v_mul_u32_u24_e32 v2, 0x147b, v2
	v_lshrrev_b32_e32 v2, 17, v2
	v_lshlrev_b32_e32 v3, 2, v1
	v_mad_u32_u24 v3, v2, s8, v3
	global_load_dword v18, v3, s[2:3] nt
	v_mul_u32_u24_e32 v4, 0x90, v1
	v_mad_i32_i24 v43, v2, s9, v4
	v_add_u32_e32 v1, 0xb00, v0
	v_lshrrev_b16_e32 v2, 2, v1
	v_mul_u32_u24_e32 v2, 0x147b, v2
	v_lshrrev_b32_e32 v2, 17, v2
	v_lshlrev_b32_e32 v3, 2, v1
	v_mad_u32_u24 v3, v2, s8, v3
	global_load_dword v19, v3, s[2:3] nt
	v_mul_u32_u24_e32 v4, 0x90, v1
	v_mad_i32_i24 v44, v2, s9, v4
	v_add_u32_e32 v1, 0xc00, v0
	v_lshrrev_b16_e32 v2, 2, v1
	v_mul_u32_u24_e32 v2, 0x147b, v2
	v_lshrrev_b32_e32 v2, 17, v2
	v_lshlrev_b32_e32 v3, 2, v1
	v_mad_u32_u24 v3, v2, s8, v3
	global_load_dword v20, v3, s[2:3] nt
	v_mul_u32_u24_e32 v4, 0x90, v1
	v_mad_i32_i24 v45, v2, s9, v4
	v_add_u32_e32 v1, 0xd00, v0
	v_lshrrev_b16_e32 v2, 2, v1
	v_mul_u32_u24_e32 v2, 0x147b, v2
	v_lshrrev_b32_e32 v2, 17, v2
	v_lshlrev_b32_e32 v3, 2, v1
	v_mad_u32_u24 v3, v2, s8, v3
	global_load_dword v21, v3, s[2:3] nt
	v_mul_u32_u24_e32 v4, 0x90, v1
	v_mad_i32_i24 v46, v2, s9, v4
	v_add_u32_e32 v1, 0xe00, v0
	v_lshrrev_b16_e32 v2, 2, v1
	v_mul_u32_u24_e32 v2, 0x147b, v2
	v_lshrrev_b32_e32 v2, 17, v2
	v_lshlrev_b32_e32 v3, 2, v1
	v_mad_u32_u24 v3, v2, s8, v3
	global_load_dword v22, v3, s[2:3] nt
	v_mul_u32_u24_e32 v4, 0x90, v1
	v_mad_i32_i24 v47, v2, s9, v4
	v_add_u32_e32 v1, 0xf00, v0
	v_lshrrev_b16_e32 v2, 2, v1
	v_mul_u32_u24_e32 v2, 0x147b, v2
	v_lshrrev_b32_e32 v2, 17, v2
	v_lshlrev_b32_e32 v3, 2, v1
	v_mad_u32_u24 v3, v2, s8, v3
	global_load_dword v23, v3, s[2:3] nt
	v_mul_u32_u24_e32 v4, 0x90, v1
	v_mad_i32_i24 v48, v2, s9, v4
	v_add_u32_e32 v1, 0x1000, v0
	v_lshrrev_b16_e32 v2, 2, v1
	v_mul_u32_u24_e32 v2, 0x147b, v2
	v_lshrrev_b32_e32 v2, 17, v2
	v_lshlrev_b32_e32 v3, 2, v1
	v_mad_u32_u24 v3, v2, s8, v3
	global_load_dword v24, v3, s[2:3] nt
	v_mul_u32_u24_e32 v4, 0x90, v1
	v_mad_i32_i24 v49, v2, s9, v4
	v_add_u32_e32 v1, 0x1100, v0
	v_lshrrev_b16_e32 v2, 2, v1
	v_mul_u32_u24_e32 v2, 0x147b, v2
	v_lshrrev_b32_e32 v2, 17, v2
	v_lshlrev_b32_e32 v3, 2, v1
	v_mad_u32_u24 v3, v2, s8, v3
	global_load_dword v25, v3, s[2:3] nt
	v_mul_u32_u24_e32 v4, 0x90, v1
	v_mad_i32_i24 v50, v2, s9, v4
	v_add_u32_e32 v1, 0x1200, v0
	v_lshrrev_b16_e32 v2, 2, v1
	v_mul_u32_u24_e32 v2, 0x147b, v2
	v_lshrrev_b32_e32 v2, 17, v2
	v_lshlrev_b32_e32 v3, 2, v1
	v_mad_u32_u24 v3, v2, s8, v3
	global_load_dword v26, v3, s[2:3] nt
	v_mul_u32_u24_e32 v4, 0x90, v1
	v_mad_i32_i24 v51, v2, s9, v4
	v_add_u32_e32 v1, 0x1300, v0
	v_lshrrev_b16_e32 v2, 2, v1
	v_mul_u32_u24_e32 v2, 0x147b, v2
	v_lshrrev_b32_e32 v2, 17, v2
	v_lshlrev_b32_e32 v3, 2, v1
	v_mad_u32_u24 v3, v2, s8, v3
	global_load_dword v27, v3, s[2:3] nt
	v_mul_u32_u24_e32 v4, 0x90, v1
	v_mad_i32_i24 v52, v2, s9, v4
	v_add_u32_e32 v1, 0x1400, v0
	v_lshrrev_b16_e32 v2, 2, v1
	v_mul_u32_u24_e32 v2, 0x147b, v2
	v_lshrrev_b32_e32 v2, 17, v2
	v_lshlrev_b32_e32 v3, 2, v1
	v_mad_u32_u24 v3, v2, s8, v3
	global_load_dword v28, v3, s[2:3] nt
	v_mul_u32_u24_e32 v4, 0x90, v1
	v_mad_i32_i24 v53, v2, s9, v4
	v_add_u32_e32 v1, 0x1500, v0
	v_lshrrev_b16_e32 v2, 2, v1
	v_mul_u32_u24_e32 v2, 0x147b, v2
	v_lshrrev_b32_e32 v2, 17, v2
	v_lshlrev_b32_e32 v3, 2, v1
	v_mad_u32_u24 v3, v2, s8, v3
	global_load_dword v29, v3, s[2:3] nt
	v_mul_u32_u24_e32 v4, 0x90, v1
	v_mad_i32_i24 v54, v2, s9, v4
	v_add_u32_e32 v1, 0x1600, v0
	v_lshrrev_b16_e32 v2, 2, v1
	v_mul_u32_u24_e32 v2, 0x147b, v2
	v_lshrrev_b32_e32 v2, 17, v2
	v_lshlrev_b32_e32 v3, 2, v1
	v_mad_u32_u24 v3, v2, s8, v3
	global_load_dword v30, v3, s[2:3] nt
	v_mul_u32_u24_e32 v4, 0x90, v1
	v_mad_i32_i24 v55, v2, s9, v4
	v_add_u32_e32 v1, 0x1700, v0
	v_lshrrev_b16_e32 v2, 2, v1
	v_mul_u32_u24_e32 v2, 0x147b, v2
	v_lshrrev_b32_e32 v2, 17, v2
	v_lshlrev_b32_e32 v3, 2, v1
	v_mad_u32_u24 v3, v2, s8, v3
	global_load_dword v31, v3, s[2:3] nt
	v_mul_u32_u24_e32 v4, 0x90, v1
	v_mad_i32_i24 v56, v2, s9, v4
	v_add_u32_e32 v1, 0x1800, v0
	v_lshrrev_b16_e32 v2, 2, v1
	v_mul_u32_u24_e32 v2, 0x147b, v2
	v_lshrrev_b32_e32 v2, 17, v2
	v_lshlrev_b32_e32 v3, 2, v1
	v_mad_u32_u24 v3, v2, s8, v3
	global_load_dword v32, v3, s[2:3] nt
	v_mul_u32_u24_e32 v4, 0x90, v1
	v_mad_i32_i24 v57, v2, s9, v4
	s_waitcnt vmcnt(24)
	v_fma_mixlo_f16 v1, v8, s10, 0
	ds_write_b16 v33, v1
	s_waitcnt vmcnt(23)
	v_fma_mixlo_f16 v2, v9, s10, 0
	ds_write_b16 v34, v2
	s_waitcnt vmcnt(22)
	v_fma_mixlo_f16 v3, v10, s10, 0
	ds_write_b16 v35, v3
	s_waitcnt vmcnt(21)
	v_fma_mixlo_f16 v4, v11, s10, 0
	ds_write_b16 v36, v4
	s_waitcnt vmcnt(20)
	v_fma_mixlo_f16 v1, v12, s10, 0
	ds_write_b16 v37, v1
	s_waitcnt vmcnt(19)
	v_fma_mixlo_f16 v2, v13, s10, 0
	ds_write_b16 v38, v2
	s_waitcnt vmcnt(18)
	v_fma_mixlo_f16 v3, v14, s10, 0
	ds_write_b16 v39, v3
	s_waitcnt vmcnt(17)
	v_fma_mixlo_f16 v4, v15, s10, 0
	ds_write_b16 v40, v4
	s_waitcnt vmcnt(16)
	v_fma_mixlo_f16 v1, v16, s10, 0
	ds_write_b16 v41, v1
	s_waitcnt vmcnt(15)
	v_fma_mixlo_f16 v2, v17, s10, 0
	ds_write_b16 v42, v2
	s_waitcnt vmcnt(14)
	v_fma_mixlo_f16 v3, v18, s10, 0
	ds_write_b16 v43, v3
	s_waitcnt vmcnt(13)
	v_fma_mixlo_f16 v4, v19, s10, 0
	ds_write_b16 v44, v4
	s_waitcnt vmcnt(12)
	v_fma_mixlo_f16 v1, v20, s10, 0
	ds_write_b16 v45, v1
	s_waitcnt vmcnt(11)
	v_fma_mixlo_f16 v2, v21, s10, 0
	ds_write_b16 v46, v2
	s_waitcnt vmcnt(10)
	v_fma_mixlo_f16 v3, v22, s10, 0
	ds_write_b16 v47, v3
	s_waitcnt vmcnt(9)
	v_fma_mixlo_f16 v4, v23, s10, 0
	ds_write_b16 v48, v4
	s_waitcnt vmcnt(8)
	v_fma_mixlo_f16 v1, v24, s10, 0
	ds_write_b16 v49, v1
	s_waitcnt vmcnt(7)
	v_fma_mixlo_f16 v2, v25, s10, 0
	ds_write_b16 v50, v2
	s_waitcnt vmcnt(6)
	v_fma_mixlo_f16 v3, v26, s10, 0
	ds_write_b16 v51, v3
	s_waitcnt vmcnt(5)
	v_fma_mixlo_f16 v4, v27, s10, 0
	ds_write_b16 v52, v4
	s_waitcnt vmcnt(4)
	v_fma_mixlo_f16 v1, v28, s10, 0
	ds_write_b16 v53, v1
	s_waitcnt vmcnt(3)
	v_fma_mixlo_f16 v2, v29, s10, 0
	ds_write_b16 v54, v2
	s_waitcnt vmcnt(2)
	v_fma_mixlo_f16 v3, v30, s10, 0
	ds_write_b16 v55, v3
	s_waitcnt vmcnt(1)
	v_fma_mixlo_f16 v4, v31, s10, 0
	ds_write_b16 v56, v4
	s_waitcnt vmcnt(0)
	v_fma_mixlo_f16 v1, v32, s10, 0
	ds_write_b16 v57, v1
	s_movk_i32 s0, 0x320
	v_cmp_gt_u32_e32 vcc, s0, v0
	s_waitcnt lgkmcnt(0)
	s_barrier
	s_and_saveexec_b64 s[0:1], vcc
	s_cbranch_execz .LBB0_61
	s_mulk_i32 s7, 0x3200
	s_add_i32 s6, s6, s7
	v_lshrrev_b32_e32 v3, 3, v0
	v_lshl_add_u32 v4, v3, 7, s6
	v_or_b32_e32 v2, 0xffffff00, v0
	v_ashrrev_i32_e32 v5, 31, v4
	v_and_b32_e32 v0, 7, v0
	v_lshlrev_b64 v[4:5], 7, v[4:5]
	v_lshlrev_b32_e32 v6, 4, v0
	v_or_b32_e32 v4, v4, v6
	s_movk_i32 s0, 0x90
	v_lshl_add_u64 v[0:1], s[4:5], 0, v[4:5]
	v_mad_u32_u24 v3, v3, s0, v6
	s_mov_b64 s[0:1], 0
	s_mov_b64 s[2:3], 0x80000
	s_movk_i32 s4, 0x21f

	.amdhsa_kernel _Z10prep_all_kPKfS0_S0_S0_S0_S0_PDF16_S1_S1_S1_S1_S1_S0_S0_S0_S0_S1_Pj
		.amdhsa_group_segment_fixed_size 14400
		.amdhsa_private_segment_fixed_size 0
		.amdhsa_kernarg_size 144
		.amdhsa_user_sgpr_count 2
		.amdhsa_user_sgpr_dispatch_ptr 0
		.amdhsa_user_sgpr_queue_ptr 0
		.amdhsa_user_sgpr_kernarg_segment_ptr 1
		.amdhsa_user_sgpr_dispatch_id 0
		.amdhsa_user_sgpr_kernarg_preload_length 0
		.amdhsa_user_sgpr_kernarg_preload_offset 0
		.amdhsa_user_sgpr_private_segment_size 0
		.amdhsa_uses_dynamic_stack 0
		.amdhsa_enable_private_segment 0
		.amdhsa_system_sgpr_workgroup_id_x 1
		.amdhsa_system_sgpr_workgroup_id_y 0
		.amdhsa_system_sgpr_workgroup_id_z 0
		.amdhsa_system_sgpr_workgroup_info 0
		.amdhsa_system_vgpr_workitem_id 0
		.amdhsa_next_free_vgpr 64
		.amdhsa_next_free_sgpr 21
		.amdhsa_accum_offset 64
		.amdhsa_reserve_vcc 1
		.amdhsa_float_round_mode_32 0
		.amdhsa_float_round_mode_16_64 0
		.amdhsa_float_denorm_mode_32 3
		.amdhsa_float_denorm_mode_16_64 3
		.amdhsa_dx10_clamp 1
		.amdhsa_ieee_mode 1
		.amdhsa_fp16_overflow 0
		.amdhsa_tg_split 0
		.amdhsa_exception_fp_ieee_invalid_op 0
		.amdhsa_exception_fp_denorm_src 0
		.amdhsa_exception_fp_ieee_div_zero 0
		.amdhsa_exception_fp_ieee_overflow 0
		.amdhsa_exception_fp_ieee_underflow 0
		.amdhsa_exception_fp_ieee_inexact 0
		.amdhsa_exception_int_div_zero 0
	.end_amdhsa_kernel

.Lc1_loop:
	s_waitcnt vmcnt(2)
	s_barrier
	s_waitcnt lgkmcnt(5)
	v_mfma_f32_16x16x32_f16 v[92:95], v[40:43], v[56:59], v[92:95]
	ds_read_b128 v[116:119], v115
	v_mfma_f32_16x16x32_f16 v[88:91], v[48:51], v[56:59], v[88:91]
	v_xor_b32_e32 v152, 64, v113
	s_waitcnt lgkmcnt(5)
	v_mfma_f32_16x16x32_f16 v[60:63], v[40:43], v[52:55], v[60:63]
	ds_read_b128 v[120:123], v115 offset:2048
	v_mfma_f32_16x16x32_f16 v[44:47], v[48:51], v[52:55], v[44:47]
	v_xor_b32_e32 v153, 64, v114
	s_mov_b32 m0, s42
	s_add_i32 s16, s13, 0xffff8000
	global_load_lds_dwordx4 v[148:149], off
	s_waitcnt lgkmcnt(5)
	v_mfma_f32_16x16x32_f16 v[28:31], v[40:43], v[64:67], v[28:31]
	ds_read_b128 v[124:127], v152
	v_mfma_f32_16x16x32_f16 v[24:27], v[48:51], v[64:67], v[24:27]
	s_and_b32 s16, s16, 0xc000
	s_add_i32 s43, s42, 0x400
	s_waitcnt lgkmcnt(5)
	v_mfma_f32_16x16x32_f16 v[12:15], v[40:43], v[68:71], v[12:15]
	ds_read_b128 v[128:131], v152 offset:2048
	v_mfma_f32_16x16x32_f16 v[8:11], v[48:51], v[68:71], v[8:11]
	v_add_u32_e32 v154, s16, v110
	s_waitcnt lgkmcnt(5)
	v_mfma_f32_16x16x32_f16 v[84:87], v[76:79], v[56:59], v[84:87]
	ds_read_b128 v[132:135], v153
	s_waitcnt lgkmcnt(5)
	v_mfma_f32_16x16x32_f16 v[72:75], v[80:83], v[56:59], v[72:75]
	v_mfma_f32_16x16x32_f16 v[36:39], v[76:79], v[52:55], v[36:39]
	ds_read_b128 v[136:139], v153 offset:2048
	v_mfma_f32_16x16x32_f16 v[32:35], v[80:83], v[52:55], v[32:35]
	v_add_u32_e32 v155, s41, v98
	v_mfma_f32_16x16x32_f16 v[20:23], v[76:79], v[64:67], v[20:23]
	ds_read_b128 v[140:143], v115 offset:4096
	v_mfma_f32_16x16x32_f16 v[16:19], v[80:83], v[64:67], v[16:19]
	v_lshlrev_b32_e32 v156, 7, v155
	v_bitop3_b32 v155, v155, v99, 6 bitop3:0x6c
	v_mfma_f32_16x16x32_f16 v[4:7], v[76:79], v[68:71], v[4:7]
	ds_read_b128 v[144:147], v115 offset:6144
	v_mfma_f32_16x16x32_f16 v[0:3], v[80:83], v[68:71], v[0:3]
	v_lshl_or_b32 v113, v155, 4, v156
	v_add_u32_e32 v115, s16, v111
	s_waitcnt lgkmcnt(5)
	v_mfma_f32_16x16x32_f16 v[92:95], v[116:119], v[124:127], v[92:95]
	ds_read_b128 v[40:43], v154
	v_mfma_f32_16x16x32_f16 v[88:91], v[120:123], v[124:127], v[88:91]
	s_mov_b32 m0, s43
	s_add_i32 s40, s40, 1
	global_load_lds_dwordx4 v[150:151], off
	s_waitcnt lgkmcnt(5)
	v_mfma_f32_16x16x32_f16 v[60:63], v[116:119], v[128:131], v[60:63]
	ds_read_b128 v[48:51], v154 offset:2048
	v_mfma_f32_16x16x32_f16 v[44:47], v[120:123], v[128:131], v[44:47]
	v_add_u32_e32 v155, s41, v109
	s_waitcnt lgkmcnt(5)
	v_mfma_f32_16x16x32_f16 v[28:31], v[116:119], v[132:135], v[28:31]
	ds_read_b128 v[56:59], v113
	v_mfma_f32_16x16x32_f16 v[24:27], v[120:123], v[132:135], v[24:27]
	v_lshlrev_b32_e32 v156, 7, v155
	v_bitop3_b32 v155, v155, v99, 6 bitop3:0x6c
	s_waitcnt lgkmcnt(5)
	v_mfma_f32_16x16x32_f16 v[12:15], v[116:119], v[136:139], v[12:15]
	ds_read_b128 v[52:55], v113 offset:2048
	v_mfma_f32_16x16x32_f16 v[8:11], v[120:123], v[136:139], v[8:11]
	v_lshl_or_b32 v114, v155, 4, v156
	s_waitcnt lgkmcnt(5)
	v_mfma_f32_16x16x32_f16 v[84:87], v[140:143], v[124:127], v[84:87]
	ds_read_b128 v[64:67], v114
	s_waitcnt lgkmcnt(5)
	v_mfma_f32_16x16x32_f16 v[72:75], v[144:147], v[124:127], v[72:75]
	s_cmp_lg_u32 s40, 20
	s_cselect_b32 s44, 1, 32
	s_cselect_b32 s40, s40, 0
	s_add_i32 s41, s41, s44
	v_mfma_f32_16x16x32_f16 v[36:39], v[140:143], v[128:131], v[36:39]
	ds_read_b128 v[68:71], v114 offset:2048
	v_mfma_f32_16x16x32_f16 v[32:35], v[144:147], v[128:131], v[32:35]
	s_addk_i32 s13, 0x4000
	s_add_i32 s14, s14, 1
	s_add_i32 s4, s14, 3
	s_cmpk_lt_u32 s14, 0x61
	s_cselect_b32 s4, s4, 0x63
	s_add_i32 s4, s4, s12
	s_lshl_b32 s4, s4, 14
	v_mfma_f32_16x16x32_f16 v[20:23], v[140:143], v[132:135], v[20:23]
	ds_read_b128 v[76:79], v154 offset:4096
	v_mfma_f32_16x16x32_f16 v[16:19], v[144:147], v[132:135], v[16:19]
	v_lshl_add_u64 v[148:149], v[100:101], 0, s[4:5]
	s_and_b32 s42, s13, 0xc000
	s_add_i32 s42, s42, s27
	v_mfma_f32_16x16x32_f16 v[4:7], v[140:143], v[136:139], v[4:7]
	ds_read_b128 v[80:83], v154 offset:6144
	v_lshl_add_u64 v[150:151], v[148:149], 0, s[8:9]
	s_cmpk_eq_i32 s14, 0x64
	v_mfma_f32_16x16x32_f16 v[0:3], v[144:147], v[136:139], v[0:3]
	s_cbranch_scc0 .Lc1_loop
	s_waitcnt vmcnt(0) lgkmcnt(0)
	s_cmpk_gt_u32 s34, 0x1ff
	s_barrier
	s_cbranch_scc1 .LBB3_8
	s_load_dword s0, s[0:1], 0x38
	v_lshl_or_b32 v40, s10, 6, v96
	s_movk_i32 s4, 0x110
	v_lshlrev_b32_e32 v41, 3, v99
	s_lshl_b32 s1, s11, 1
	v_mul_lo_u32 v40, v40, s4
	v_add3_u32 v48, s1, v41, v40
	v_mov_b32_e32 v40, v93
	v_mov_b32_e32 v41, v94
	s_waitcnt lgkmcnt(0)
	v_pk_mul_f32 v[40:41], s[0:1], v[40:41] op_sel_hi:[0,1]
	v_fma_mixlo_f16 v42, s0, v92, 0
	v_cvt_pk_f16_f32 v41, v40, v41
	v_pack_b32_f16 v40, v42, v41
	v_fma_mixlo_f16 v42, s0, v95, 0
	v_alignbit_b32 v41, v42, v41, 16
	v_mov_b32_e32 v42, v89
	v_mov_b32_e32 v43, v90
	v_pk_mul_f32 v[42:43], s[0:1], v[42:43] op_sel_hi:[0,1]
	v_fma_mixlo_f16 v49, s0, v88, 0
	v_cvt_pk_f16_f32 v43, v42, v43
	v_pack_b32_f16 v42, v49, v43
	v_fma_mixlo_f16 v49, s0, v91, 0
	v_alignbit_b32 v43, v49, v43, 16
	ds_write2_b64 v48, v[40:41], v[42:43] offset1:4
	v_mov_b32_e32 v40, v85
	v_mov_b32_e32 v41, v86
	v_pk_mul_f32 v[40:41], s[0:1], v[40:41] op_sel_hi:[0,1]
	v_fma_mixlo_f16 v42, s0, v84, 0
	v_cvt_pk_f16_f32 v41, v40, v41
	v_pack_b32_f16 v40, v42, v41
	v_fma_mixlo_f16 v42, s0, v87, 0
	v_alignbit_b32 v41, v42, v41, 16
	v_mov_b32_e32 v42, v73
	v_mov_b32_e32 v43, v74
	v_pk_mul_f32 v[42:43], s[0:1], v[42:43] op_sel_hi:[0,1]
	v_fma_mixlo_f16 v49, s0, v72, 0
	v_cvt_pk_f16_f32 v43, v42, v43
	v_pack_b32_f16 v42, v49, v43
	v_fma_mixlo_f16 v49, s0, v75, 0
	v_alignbit_b32 v43, v49, v43, 16
	ds_write2_b64 v48, v[40:41], v[42:43] offset0:8 offset1:12
	v_mov_b32_e32 v40, v61
	v_mov_b32_e32 v41, v62
	v_pk_mul_f32 v[40:41], s[0:1], v[40:41] op_sel_hi:[0,1]
	v_fma_mixlo_f16 v42, s0, v60, 0
	v_cvt_pk_f16_f32 v41, v40, v41
	v_pack_b32_f16 v40, v42, v41
	v_fma_mixlo_f16 v42, s0, v63, 0
	v_alignbit_b32 v41, v42, v41, 16
	v_mov_b32_e32 v42, v45
	v_mov_b32_e32 v43, v46
	v_pk_mul_f32 v[42:43], s[0:1], v[42:43] op_sel_hi:[0,1]
	v_fma_mixlo_f16 v44, s0, v44, 0
	v_cvt_pk_f16_f32 v43, v42, v43
	v_pack_b32_f16 v42, v44, v43
	v_fma_mixlo_f16 v44, s0, v47, 0
	v_alignbit_b32 v43, v44, v43, 16
	v_add_u32_e32 v44, 0x1000, v48
	ds_write2_b64 v44, v[40:41], v[42:43] offset0:32 offset1:36
	v_fma_mixlo_f16 v40, s0, v36, 0
	v_mov_b32_e32 v36, v37
	v_mov_b32_e32 v37, v38
	v_pk_mul_f32 v[36:37], s[0:1], v[36:37] op_sel_hi:[0,1]
	v_cvt_pk_f16_f32 v37, v36, v37
	v_fma_mixlo_f16 v38, s0, v39, 0
	v_pack_b32_f16 v36, v40, v37
	v_alignbit_b32 v37, v38, v37, 16
	v_fma_mixlo_f16 v38, s0, v32, 0
	v_mov_b32_e32 v32, v33
	v_mov_b32_e32 v33, v34
	v_pk_mul_f32 v[32:33], s[0:1], v[32:33] op_sel_hi:[0,1]
	v_cvt_pk_f16_f32 v33, v32, v33
	v_fma_mixlo_f16 v34, s0, v35, 0
	v_pack_b32_f16 v32, v38, v33
	v_alignbit_b32 v33, v34, v33, 16
	ds_write2_b64 v44, v[36:37], v[32:33] offset0:40 offset1:44
	v_fma_mixlo_f16 v32, s0, v28, 0
	v_mov_b32_e32 v28, v29
	v_mov_b32_e32 v29, v30
	v_pk_mul_f32 v[28:29], s[0:1], v[28:29] op_sel_hi:[0,1]
	v_cvt_pk_f16_f32 v29, v28, v29
	v_fma_mixlo_f16 v30, s0, v31, 0
	v_pack_b32_f16 v28, v32, v29
	v_alignbit_b32 v29, v30, v29, 16
	v_fma_mixlo_f16 v30, s0, v24, 0
	v_mov_b32_e32 v24, v25
	v_mov_b32_e32 v25, v26
	v_pk_mul_f32 v[24:25], s[0:1], v[24:25] op_sel_hi:[0,1]
	v_cvt_pk_f16_f32 v25, v24, v25
	v_fma_mixlo_f16 v26, s0, v27, 0
	v_pack_b32_f16 v24, v30, v25
	v_alignbit_b32 v25, v26, v25, 16
	v_add_u32_e32 v26, 0x2000, v48
	ds_write2_b64 v26, v[28:29], v[24:25] offset0:64 offset1:68
	v_fma_mixlo_f16 v24, s0, v20, 0
	v_mov_b32_e32 v20, v21
	v_mov_b32_e32 v21, v22
	v_pk_mul_f32 v[20:21], s[0:1], v[20:21] op_sel_hi:[0,1]
	v_cvt_pk_f16_f32 v21, v20, v21
	v_fma_mixlo_f16 v22, s0, v23, 0
	v_pack_b32_f16 v20, v24, v21
	v_alignbit_b32 v21, v22, v21, 16
	v_fma_mixlo_f16 v22, s0, v16, 0
	v_mov_b32_e32 v16, v17
	v_mov_b32_e32 v17, v18
	v_pk_mul_f32 v[16:17], s[0:1], v[16:17] op_sel_hi:[0,1]
	v_cvt_pk_f16_f32 v17, v16, v17
	v_fma_mixlo_f16 v18, s0, v19, 0
	v_pack_b32_f16 v16, v22, v17
	v_alignbit_b32 v17, v18, v17, 16
	ds_write2_b64 v26, v[20:21], v[16:17] offset0:72 offset1:76
	v_fma_mixlo_f16 v16, s0, v12, 0
	v_mov_b32_e32 v12, v13
	v_mov_b32_e32 v13, v14
	v_pk_mul_f32 v[12:13], s[0:1], v[12:13] op_sel_hi:[0,1]
	v_cvt_pk_f16_f32 v13, v12, v13
	v_fma_mixlo_f16 v14, s0, v15, 0
	v_pack_b32_f16 v12, v16, v13
	v_alignbit_b32 v13, v14, v13, 16
	v_fma_mixlo_f16 v14, s0, v8, 0
	v_mov_b32_e32 v8, v9
	v_mov_b32_e32 v9, v10
	v_pk_mul_f32 v[8:9], s[0:1], v[8:9] op_sel_hi:[0,1]
	v_cvt_pk_f16_f32 v9, v8, v9
	v_fma_mixlo_f16 v10, s0, v11, 0
	v_pack_b32_f16 v8, v14, v9
	v_alignbit_b32 v9, v10, v9, 16
	v_add_u32_e32 v10, 0x3000, v48
	ds_write2_b64 v10, v[12:13], v[8:9] offset0:96 offset1:100
	v_fma_mixlo_f16 v8, s0, v4, 0
	v_mov_b32_e32 v4, v5
	v_mov_b32_e32 v5, v6
	v_pk_mul_f32 v[4:5], s[0:1], v[4:5] op_sel_hi:[0,1]
	v_cvt_pk_f16_f32 v5, v4, v5
	v_fma_mixlo_f16 v6, s0, v7, 0
	v_pack_b32_f16 v4, v8, v5
	v_alignbit_b32 v5, v6, v5, 16
	v_fma_mixlo_f16 v6, s0, v0, 0
	v_mov_b32_e32 v0, v1
	v_mov_b32_e32 v1, v2
	v_pk_mul_f32 v[0:1], s[0:1], v[0:1] op_sel_hi:[0,1]
	v_cvt_pk_f16_f32 v1, v0, v1
	v_fma_mixlo_f16 v2, s0, v3, 0
	v_pack_b32_f16 v0, v6, v1
	v_alignbit_b32 v1, v2, v1, 16
	ds_write2_b64 v10, v[4:5], v[0:1] offset0:104 offset1:108

_Z6conv_kILi256ELi512ELi3ELi128ELi1ELi1ELb0EEvPKDF16_S1_PKfS3_PDF16_S4_S1_fS3_S3_S3_S3_:
	s_lshl_b32 s3, s2, 3
	s_load_dwordx2 s[36:37], s[0:1], 0x0
	s_load_dwordx4 s[4:7], s[0:1], 0x10
	s_load_dwordx2 s[30:31], s[0:1], 0x30
	s_and_b32 s3, s3, 56
	s_ashr_i32 s8, s2, 5
	s_add_i32 s3, s3, s8
	v_readfirstlane_b32 s40, v0
	s_lshl_b32 s8, s3, 2
	s_bfe_u32 s49, s2, 0x20003
	s_and_b32 s33, s8, 56
	s_lshr_b32 s50, s40, 6
	s_bfe_u32 s41, s40, 0x10006
	s_ashr_i32 s38, s3, 4
	s_and_b32 s27, s2, 32
	s_lshl_b32 s2, s49, 9
	s_waitcnt lgkmcnt(0)
	s_add_u32 s2, s4, s2
	s_addc_u32 s3, s5, 0
	s_lshl_b32 s4, s41, 8
	s_add_u32 s2, s2, s4
	s_addc_u32 s3, s3, 0
	v_and_b32_e32 v18, 48, v0
	v_mov_b32_e32 v19, 0
	v_lshl_add_u64 v[2:3], s[2:3], 0, v[18:19]
	s_load_dword s26, s[6:7], 0x0
	global_load_dwordx4 v[14:17], v[2:3], off
	v_lshl_add_u64 v[4:5], v[2:3], 0, 64
	s_mov_b64 s[2:3], 0x80
	v_bfe_u32 v28, v0, 3, 3
	v_and_b32_e32 v1, 7, v0
	global_load_dwordx4 v[10:13], v[4:5], off
	v_lshl_add_u64 v[4:5], v[2:3], 0, s[2:3]
	s_mov_b64 s[2:3], 0xc0
	v_bitop3_b32 v1, v28, v1, 6 bitop3:0x6c
	v_lshl_add_u64 v[2:3], v[2:3], 0, s[2:3]
	v_lshl_or_b32 v18, s50, 3, v28
	s_mov_b32 s2, 0x1e1e1e1f
	v_lshlrev_b32_e32 v20, 3, v1
	v_mul_hi_u32 v1, v18, s2
	v_lshrrev_b32_e32 v21, 2, v1
	s_movk_i32 s8, 0xffde
	s_add_i32 s24, s33, -1
	global_load_dwordx4 v[6:9], v[4:5], off
	v_mul_lo_u32 v22, v21, s8
	v_add_u32_e32 v1, s24, v21
	s_add_i32 s25, s27, -1
	s_movk_i32 s9, 0x154
	global_load_dwordx4 v[2:5], v[2:3], off
	v_add3_u32 v24, s25, v18, v22
	v_cmp_gt_u32_e64 s[2:3], s9, v18
	v_cmp_gt_u32_e32 vcc, 64, v1
	s_and_b64 s[6:7], s[2:3], vcc
	v_cmp_gt_u32_e64 s[4:5], 64, v24
	v_and_b32_e32 v25, 63, v0
	s_and_b64 s[10:11], s[6:7], s[4:5]
	v_mov_b64_e32 v[22:23], s[30:31]
	v_lshlrev_b32_e32 v18, 1, v20
	s_and_saveexec_b64 s[6:7], s[10:11]
	s_lshl_b32 s10, s38, 14
	v_lshlrev_b32_e32 v1, 6, v1
	v_or3_b32 v22, v1, s10, v24
	v_ashrrev_i32_e32 v23, 31, v22
	v_lshlrev_b64 v[22:23], 7, v[22:23]
	v_lshl_add_u64 v[22:23], s[36:37], 0, v[22:23]
	v_lshl_add_u64 v[22:23], v[22:23], 0, v[18:19]
	s_or_b64 exec, exec, s[6:7]
	s_lshl_b32 s42, s50, 10
	v_lshlrev_b32_e32 v1, 4, v25
	v_or_b32_e32 v19, s42, v1
	s_add_i32 s13, s50, 8
	v_readfirstlane_b32 s6, v19
	s_mov_b32 m0, s6
	s_mov_b32 s12, 0x3c3c3c3d
	global_load_lds_dwordx4 v[22:23], off
	v_lshl_or_b32 v22, s13, 3, v28
	v_mul_hi_u32 v19, v22, s12
	v_lshrrev_b32_e32 v26, 3, v19
	v_mul_lo_u32 v23, v26, s8
	v_add_u32_e32 v19, s24, v26
	v_add3_u32 v27, s25, v22, v23
	v_cmp_gt_u32_e64 s[6:7], s9, v22
	v_cmp_gt_u32_e32 vcc, 64, v19
	s_and_b64 s[10:11], s[6:7], vcc
	v_cmp_gt_u32_e64 s[8:9], 64, v27
	s_and_b64 s[14:15], s[10:11], s[8:9]
	v_mov_b64_e32 v[22:23], s[30:31]
	s_and_saveexec_b64 s[10:11], s[14:15]
	s_lshl_b32 s14, s38, 14
	v_lshlrev_b32_e32 v19, 6, v19
	v_or3_b32 v22, v19, s14, v27
	v_ashrrev_i32_e32 v23, 31, v22
	v_lshlrev_b64 v[22:23], 7, v[22:23]
	v_lshl_add_u64 v[22:23], s[36:37], 0, v[22:23]
	v_mov_b32_e32 v19, 0
	v_lshl_add_u64 v[22:23], v[22:23], 0, v[18:19]
	s_or_b64 exec, exec, s[10:11]
	s_lshl_b32 s43, s13, 10
	v_or_b32_e32 v19, s43, v1
	s_add_i32 s18, s50, 16
	v_readfirstlane_b32 s10, v19
	s_mov_b32 m0, s10
	s_movk_i32 s16, 0xffde
	global_load_lds_dwordx4 v[22:23], off
	v_lshl_or_b32 v22, s18, 3, v28
	v_mul_hi_u32 v19, v22, s12
	v_lshrrev_b32_e32 v29, 3, v19
	v_mul_lo_u32 v23, v29, s16
	v_add_u32_e32 v19, s24, v29
	s_movk_i32 s17, 0x154
	v_add3_u32 v30, s25, v22, v23
	v_cmp_gt_u32_e64 s[10:11], s17, v22
	v_cmp_gt_u32_e32 vcc, 64, v19
	s_and_b64 s[14:15], s[10:11], vcc
	v_cmp_gt_u32_e64 s[12:13], 64, v30
	s_and_b64 s[20:21], s[14:15], s[12:13]
	v_mov_b64_e32 v[22:23], s[30:31]
	s_and_saveexec_b64 s[14:15], s[20:21]
	s_lshl_b32 s19, s38, 14
	v_lshlrev_b32_e32 v19, 6, v19
	v_or3_b32 v22, v19, s19, v30
	v_ashrrev_i32_e32 v23, 31, v22
	v_lshlrev_b64 v[22:23], 7, v[22:23]
	v_lshl_add_u64 v[22:23], s[36:37], 0, v[22:23]
	v_mov_b32_e32 v19, 0
	v_lshl_add_u64 v[22:23], v[22:23], 0, v[18:19]
	s_or_b64 exec, exec, s[14:15]
	s_lshl_b32 s44, s18, 10
	v_or_b32_e32 v19, s44, v1
	s_add_i32 s21, s50, 24
	v_readfirstlane_b32 s14, v19
	s_mov_b32 m0, s14
	s_mov_b32 s20, 0x3c3c3c3d
	global_load_lds_dwordx4 v[22:23], off
	v_lshl_or_b32 v22, s21, 3, v28
	v_mul_hi_u32 v19, v22, s20
	v_lshrrev_b32_e32 v31, 3, v19
	v_mul_lo_u32 v23, v31, s16
	v_add_u32_e32 v19, s24, v31
	v_add3_u32 v32, s25, v22, v23
	v_cmp_gt_u32_e64 s[14:15], s17, v22
	v_cmp_gt_u32_e32 vcc, 64, v19
	s_and_b64 s[18:19], s[14:15], vcc
	v_cmp_gt_u32_e64 s[16:17], 64, v32
	s_and_b64 s[22:23], s[18:19], s[16:17]
	v_mov_b64_e32 v[22:23], s[30:31]
	s_and_saveexec_b64 s[18:19], s[22:23]
	s_lshl_b32 s22, s38, 14
	v_lshlrev_b32_e32 v19, 6, v19
	v_or3_b32 v22, v19, s22, v32
	v_ashrrev_i32_e32 v23, 31, v22
	v_lshlrev_b64 v[22:23], 7, v[22:23]
	v_lshl_add_u64 v[22:23], s[36:37], 0, v[22:23]
	v_mov_b32_e32 v19, 0
	v_lshl_add_u64 v[22:23], v[22:23], 0, v[18:19]
	s_or_b64 exec, exec, s[18:19]
	s_lshl_b32 s45, s21, 10
	v_or_b32_e32 v19, s45, v1
	s_add_i32 s28, s50, 32
	v_readfirstlane_b32 s18, v19
	s_mov_b32 m0, s18
	s_movk_i32 s18, 0xffde
	global_load_lds_dwordx4 v[22:23], off
	v_lshl_or_b32 v22, s28, 3, v28
	v_mul_hi_u32 v19, v22, s20
	v_lshrrev_b32_e32 v33, 3, v19
	v_mul_lo_u32 v23, v33, s18
	v_add_u32_e32 v19, s24, v33
	s_movk_i32 s18, 0x154
	v_add3_u32 v34, s25, v22, v23
	v_cmp_gt_u32_e64 s[18:19], s18, v22
	v_cmp_gt_u32_e32 vcc, 64, v19
	s_and_b64 s[22:23], s[18:19], vcc
	v_cmp_gt_u32_e64 s[20:21], 64, v34
	s_and_b64 s[22:23], s[22:23], s[20:21]
	s_xor_b64 s[22:23], s[22:23], -1
	s_and_saveexec_b64 s[34:35], s[22:23]
	s_xor_b64 s[22:23], exec, s[34:35]
	s_lshl_b32 s29, s38, 14
	s_or_saveexec_b64 s[22:23], s[22:23]
	v_mov_b32_e32 v35, s29
	v_mov_b64_e32 v[22:23], s[30:31]
	s_xor_b64 exec, exec, s[22:23]
	s_lshl_b32 s29, s38, 14
	v_lshlrev_b32_e32 v19, 6, v19
	v_or3_b32 v22, v19, s29, v34
	v_ashrrev_i32_e32 v23, 31, v22
	v_lshlrev_b64 v[22:23], 7, v[22:23]
	v_lshl_add_u64 v[22:23], s[36:37], 0, v[22:23]
	v_mov_b32_e32 v19, 0
	v_lshl_add_u64 v[22:23], v[22:23], 0, v[18:19]
	v_mov_b32_e32 v35, s29
	s_or_b64 exec, exec, s[22:23]
	s_lshl_b32 s46, s28, 10
	v_or_b32_e32 v18, s46, v1
	s_add_i32 s48, s50, 40
	v_readfirstlane_b32 s22, v18
	s_mov_b32 m0, s22
	v_lshl_or_b32 v19, s48, 3, v28
	global_load_lds_dwordx4 v[22:23], off
	s_mov_b32 s22, 0x3c3c3c3d
	v_mul_hi_u32 v18, v19, s22
	v_lshrrev_b32_e32 v36, 3, v18
	s_movk_i32 s22, 0xffde
	s_load_dwordx2 s[34:35], s[0:1], 0x8
	v_mul_lo_u32 v22, v36, s22
	v_add_u32_e32 v18, s24, v36
	s_movk_i32 s22, 0x154
	v_add3_u32 v37, s25, v19, v22
	v_cmp_gt_u32_e64 s[22:23], s22, v19
	v_cmp_gt_u32_e32 vcc, 64, v18
	s_and_b64 s[28:29], s[22:23], vcc
	v_cmp_gt_u32_e64 s[24:25], 64, v37
	s_and_b64 s[28:29], s[28:29], s[24:25]
	s_xor_b64 s[28:29], s[28:29], -1
	s_and_saveexec_b64 s[52:53], s[28:29]
	s_xor_b64 s[28:29], exec, s[52:53]
	s_or_saveexec_b64 s[28:29], s[28:29]
	s_lshl_b32 s51, s41, 6
	v_mov_b64_e32 v[22:23], s[30:31]
	s_xor_b64 exec, exec, s[28:29]
	v_lshlrev_b32_e32 v18, 6, v18
	v_or3_b32 v18, v18, v35, v37
	v_ashrrev_i32_e32 v19, 31, v18
	v_lshlrev_b64 v[18:19], 7, v[18:19]
	v_lshl_add_u64 v[18:19], s[36:37], 0, v[18:19]
	v_lshlrev_b32_e32 v22, 1, v20
	v_mov_b32_e32 v23, 0
	v_lshl_add_u64 v[22:23], v[18:19], 0, v[22:23]
	s_or_b64 exec, exec, s[28:29]
	v_and_b32_e32 v114, 15, v0
	s_and_b32 s52, s50, 6
	v_mad_u64_u32 v[116:117], s[52:53], s52, 34, v[114:115]
	v_lshrrev_b32_e32 v115, 4, v25
	v_or_b32_e32 v19, s51, v114
	v_bitop3_b32 v25, v115, v0, 6 bitop3:0x78
	v_lshlrev_b32_e32 v19, 7, v19
	v_lshlrev_b32_e32 v25, 4, v25
	s_mov_b32 s51, 0x18040
	s_lshl_b32 s48, s48, 10
	v_lshlrev_b32_e32 v18, 6, v28
	v_or_b32_e32 v28, v19, v25
	v_bitop3_b32 v125, v19, s51, v25 bitop3:0x36
	v_or_b32_e32 v19, s48, v1
	s_lshl_b32 s39, s49, 7
	v_readfirstlane_b32 s51, v19
	s_lshr_b32 s47, s40, 7
	s_mov_b32 m0, s51
	s_lshl_b32 s51, s49, 14
	s_waitcnt lgkmcnt(0)
	s_add_u32 s52, s34, s51
	v_or3_b32 v18, s42, v18, v20
	s_addc_u32 s53, s35, 0
	s_lshl_b32 s56, s50, 11
	v_mov_b32_e32 v19, 0
	global_load_lds_dwordx4 v[22:23], off
	s_add_i32 s50, s56, 0x18000
	v_lshlrev_b64 v[22:23], 1, v[18:19]
	v_lshl_add_u64 v[118:119], s[52:53], 0, v[22:23]
	s_mov_b32 m0, s50
	s_mov_b64 s[34:35], 0x400
	global_load_lds_dwordx4 v[118:119], off
	s_add_i32 m0, s56, 0x18400
	s_add_u32 s54, s52, 0x10000
	v_lshl_add_u64 v[40:41], v[118:119], 0, s[34:35]
	s_addc_u32 s55, s53, 0
	global_load_lds_dwordx4 v[40:41], off
	s_add_i32 m0, s56, 0x1c000
	v_lshl_add_u64 v[40:41], s[54:55], 0, v[22:23]
	v_or_b32_e32 v38, 0x200, v18
	v_mov_b32_e32 v39, v19
	global_load_lds_dwordx4 v[40:41], off
	s_add_i32 m0, s56, 0x1c400
	v_lshlrev_b64 v[38:39], 1, v[38:39]
	s_add_u32 s52, s52, 0x20000
	v_lshl_add_u64 v[40:41], s[54:55], 0, v[38:39]
	s_addc_u32 s53, s53, 0
	global_load_lds_dwordx4 v[40:41], off
	s_add_i32 m0, s56, 0x20000
	v_lshl_add_u64 v[22:23], s[52:53], 0, v[22:23]
	global_load_lds_dwordx4 v[22:23], off
	v_lshl_add_u64 v[22:23], s[52:53], 0, v[38:39]
	s_add_i32 m0, s56, 0x20400
	v_or_b32_e32 v124, 0x18000, v28
	global_load_lds_dwordx4 v[22:23], off
	s_waitcnt vmcnt(4) lgkmcnt(0)
	s_barrier
	ds_read_b128 v[66:69], v124
	ds_read_b128 v[70:73], v124 offset:2048
	v_lshlrev_b32_e32 v18, 7, v116
	v_bitop3_b32 v22, v116, v115, 6 bitop3:0x6c
	v_add_u32_e32 v117, 34, v116
	v_lshl_or_b32 v138, v22, 4, v18
	ds_read_b128 v[78:81], v138
	ds_read_b128 v[74:77], v138 offset:2048
	v_lshlrev_b32_e32 v18, 7, v117
	v_bitop3_b32 v22, v117, v115, 6 bitop3:0x6c
	v_lshl_or_b32 v139, v22, 4, v18
	ds_read_b128 v[82:85], v139
	s_load_dwordx2 s[28:29], s[0:1], 0x20
	ds_read_b128 v[86:89], v139 offset:2048
	ds_read_b128 v[94:97], v124 offset:4096
	ds_read_b128 v[98:101], v124 offset:6144
	v_lshlrev_b32_e32 v18, 1, v20
	s_mov_b32 s49, 0
	s_mov_b32 s51, 1
	v_add_u32_e32 v126, s33, v21
	v_add_u32_e32 v127, v35, v24
	v_lshl_add_u64 v[120:121], s[36:37], 0, v[18:19]
	v_add_u32_e32 v128, s33, v26
	v_add_u32_e32 v129, v35, v27
	v_add_u32_e32 v130, s33, v29
	v_add_u32_e32 v131, v35, v30
	v_add_u32_e32 v132, s33, v31
	v_add_u32_e32 v133, v35, v32
	v_add_u32_e32 v134, s33, v33
	v_add_u32_e32 v135, v35, v34
	v_add_u32_e32 v136, s33, v36
	v_add_u32_e32 v137, v35, v37
	s_mov_b64 s[36:37], 0
	s_mov_b32 s52, 0
	v_mov_b32_e32 v18, v19
	v_mov_b32_e32 v20, v19
	v_mov_b32_e32 v21, v19
	v_mov_b32_e32 v38, v19
	v_mov_b32_e32 v39, v19
	v_mov_b32_e32 v40, v19
	v_mov_b32_e32 v41, v19
	v_mov_b32_e32 v42, v19
	v_mov_b32_e32 v43, v19
	v_mov_b32_e32 v44, v19
	v_mov_b32_e32 v45, v19
	v_mov_b32_e32 v46, v19
	v_mov_b32_e32 v47, v19
	v_mov_b32_e32 v48, v19
	v_mov_b32_e32 v49, v19
	v_mov_b32_e32 v50, v19
	v_mov_b32_e32 v51, v19
	v_mov_b32_e32 v52, v19
	v_mov_b32_e32 v53, v19
	v_mov_b32_e32 v54, v19
	v_mov_b32_e32 v55, v19
	v_mov_b32_e32 v56, v19
	v_mov_b32_e32 v57, v19
	v_mov_b32_e32 v58, v19
	v_mov_b32_e32 v59, v19
	v_mov_b32_e32 v60, v19
	v_mov_b32_e32 v61, v19
	v_mov_b32_e32 v62, v19
	v_mov_b32_e32 v63, v19
	v_mov_b32_e32 v64, v19
	v_mov_b32_e32 v65, v19
	v_mov_b32_e32 v90, v19
	v_mov_b32_e32 v91, v19
	v_mov_b32_e32 v92, v19
	v_mov_b32_e32 v93, v19
	v_mov_b32_e32 v102, v19
	v_mov_b32_e32 v103, v19
	v_mov_b32_e32 v104, v19
	v_mov_b32_e32 v105, v19
	v_mov_b32_e32 v106, v19
	v_mov_b32_e32 v107, v19
	v_mov_b32_e32 v108, v19
	v_mov_b32_e32 v109, v19
	v_mov_b32_e32 v110, v19
	v_mov_b32_e32 v111, v19
	v_mov_b32_e32 v112, v19
	v_mov_b32_e32 v113, v19
	v_mov_b32_e32 v34, v19
	v_mov_b32_e32 v35, v19
	v_mov_b32_e32 v36, v19
	v_mov_b32_e32 v37, v19
	v_mov_b32_e32 v30, v19
	v_mov_b32_e32 v31, v19
	v_mov_b32_e32 v32, v19
	v_mov_b32_e32 v33, v19
	v_mov_b32_e32 v26, v19
	v_mov_b32_e32 v27, v19
	v_mov_b32_e32 v28, v19
	v_mov_b32_e32 v29, v19
	v_mov_b32_e32 v22, v19
	v_mov_b32_e32 v23, v19
	v_mov_b32_e32 v24, v19
	v_mov_b32_e32 v25, v19
	s_mov_b32 s60, 0
	s_mov_b32 s61, 1
	s_mov_b32 s62, 1
	s_mov_b32 s63, 1
	s_mov_b32 s64, 0
	s_mov_b32 s66, 1
	s_mov_b32 s67, 0
	s_mov_b32 s68, 0x30000
	s_mov_b32 s69, 0
	v_lshl_add_u64 v[176:177], v[118:119], 0, s[68:69]
	s_add_i32 s70, s50, 0xc000
	v_lshl_add_u64 v[178:179], v[176:177], 0, s[34:35]
	v_mov_b32_e32 v172, v125
.Lc3_loop:
	s_cmp_eq_u32 s67, 0
	s_cbranch_scc1 .Lc3_w2
	s_waitcnt vmcnt(8)
	s_sub_i32 s67, s67, 1
	s_branch .Lc3_bar

.Lc3_bar:
	s_barrier
	s_waitcnt lgkmcnt(5)
	v_mfma_f32_16x16x32_f16 v[110:113], v[66:69], v[78:81], v[110:113]
	ds_read_b128 v[140:143], v172
	v_mfma_f32_16x16x32_f16 v[106:109], v[70:73], v[78:81], v[106:109]
	v_xor_b32_e32 v174, 64, v138
	s_waitcnt lgkmcnt(5)
	v_mfma_f32_16x16x32_f16 v[62:65], v[66:69], v[74:77], v[62:65]
	ds_read_b128 v[144:147], v172 offset:2048
	v_mfma_f32_16x16x32_f16 v[58:61], v[70:73], v[74:77], v[58:61]
	v_xor_b32_e32 v175, 64, v139
	s_mov_b32 m0, s70
	s_add_i32 s71, s49, 0x4000
	global_load_lds_dwordx4 v[176:177], off
	s_waitcnt lgkmcnt(5)
	v_mfma_f32_16x16x32_f16 v[46:49], v[66:69], v[82:85], v[46:49]
	ds_read_b128 v[148:151], v174
	v_mfma_f32_16x16x32_f16 v[42:45], v[70:73], v[82:85], v[42:45]
	s_and_b32 s71, s71, 0xc000
	s_add_i32 s72, s70, 0x400
	s_waitcnt lgkmcnt(5)
	v_mfma_f32_16x16x32_f16 v[34:37], v[66:69], v[86:89], v[34:37]
	ds_read_b128 v[152:155], v174 offset:2048
	v_mfma_f32_16x16x32_f16 v[30:33], v[70:73], v[86:89], v[30:33]
	v_add_u32_e32 v173, s71, v124
	s_waitcnt lgkmcnt(5)
	v_mfma_f32_16x16x32_f16 v[102:105], v[94:97], v[78:81], v[102:105]
	ds_read_b128 v[156:159], v175
	s_waitcnt lgkmcnt(5)
	v_mfma_f32_16x16x32_f16 v[90:93], v[98:101], v[78:81], v[90:93]
	v_mfma_f32_16x16x32_f16 v[54:57], v[94:97], v[74:77], v[54:57]
	ds_read_b128 v[160:163], v175 offset:2048
	v_mfma_f32_16x16x32_f16 v[50:53], v[98:101], v[74:77], v[50:53]
	v_add_u32_e32 v180, s62, v116
	v_mfma_f32_16x16x32_f16 v[38:41], v[94:97], v[82:85], v[38:41]
	ds_read_b128 v[164:167], v172 offset:4096
	v_mfma_f32_16x16x32_f16 v[18:21], v[98:101], v[82:85], v[18:21]
	v_bitop3_b32 v181, v180, v115, 6 bitop3:0x6c
	v_lshl_add_u32 v180, v180, 7, s64
	v_mfma_f32_16x16x32_f16 v[26:29], v[94:97], v[86:89], v[26:29]
	ds_read_b128 v[168:171], v172 offset:6144
	v_mfma_f32_16x16x32_f16 v[22:25], v[98:101], v[86:89], v[22:25]
	v_lshl_or_b32 v138, v181, 4, v180
	v_add_u32_e32 v172, s71, v125
	s_waitcnt lgkmcnt(5)
	v_mfma_f32_16x16x32_f16 v[110:113], v[140:143], v[148:151], v[110:113]
	ds_read_b128 v[66:69], v173
	v_mfma_f32_16x16x32_f16 v[106:109], v[144:147], v[148:151], v[106:109]
	s_mov_b32 m0, s72
	s_add_i32 s61, s61, 1
	global_load_lds_dwordx4 v[178:179], off
	s_waitcnt lgkmcnt(5)
	v_mfma_f32_16x16x32_f16 v[62:65], v[140:143], v[152:155], v[62:65]
	ds_read_b128 v[70:73], v173 offset:2048
	v_mfma_f32_16x16x32_f16 v[58:61], v[144:147], v[152:155], v[58:61]
	v_add_u32_e32 v180, s62, v117
	s_waitcnt lgkmcnt(5)
	v_mfma_f32_16x16x32_f16 v[46:49], v[140:143], v[156:159], v[46:49]
	ds_read_b128 v[78:81], v138
	v_mfma_f32_16x16x32_f16 v[42:45], v[144:147], v[156:159], v[42:45]
	v_bitop3_b32 v181, v180, v115, 6 bitop3:0x6c
	v_lshl_add_u32 v180, v180, 7, s64
	s_waitcnt lgkmcnt(5)
	v_mfma_f32_16x16x32_f16 v[34:37], v[140:143], v[160:163], v[34:37]
	ds_read_b128 v[74:77], v138 offset:2048
	v_mfma_f32_16x16x32_f16 v[30:33], v[144:147], v[160:163], v[30:33]
	v_lshl_or_b32 v139, v181, 4, v180
	s_waitcnt lgkmcnt(5)
	v_mfma_f32_16x16x32_f16 v[102:105], v[164:167], v[148:151], v[102:105]
	ds_read_b128 v[82:85], v139
	s_waitcnt lgkmcnt(5)
	v_mfma_f32_16x16x32_f16 v[90:93], v[168:171], v[148:151], v[90:93]
	s_cmp_lg_u32 s61, 3
	s_cselect_b32 s73, 1, 32
	s_cselect_b32 s61, s61, 0
	s_add_i32 s62, s62, s73
	s_add_i32 s63, s63, 1
	v_mfma_f32_16x16x32_f16 v[54:57], v[164:167], v[152:155], v[54:57]
	ds_read_b128 v[86:89], v139 offset:2048
	s_cmp_lg_u32 s63, 9
	s_cselect_b32 s62, s62, 0
	s_cselect_b32 s63, s63, 0
	s_cselect_b32 s73, 0, 0xc000
	s_xor_b32 s64, s64, s73
	v_mfma_f32_16x16x32_f16 v[50:53], v[168:171], v[152:155], v[50:53]
	s_addk_i32 s49, 0x4000
	s_add_i32 s60, s60, 1
	s_add_i32 s74, s60, 3
	s_cmp_lt_u32 s60, 33
	s_cselect_b32 s74, s74, 35
	s_lshl_b32 s68, s74, 16
	v_mfma_f32_16x16x32_f16 v[38:41], v[164:167], v[156:159], v[38:41]
	ds_read_b128 v[94:97], v173 offset:4096
	v_mfma_f32_16x16x32_f16 v[18:21], v[168:171], v[156:159], v[18:21]
	v_lshl_add_u64 v[176:177], v[118:119], 0, s[68:69]
	s_add_i32 s70, s49, 0xc000
	s_and_b32 s70, s70, 0xc000
	s_add_i32 s70, s70, s50
	v_mfma_f32_16x16x32_f16 v[26:29], v[164:167], v[160:163], v[26:29]
	ds_read_b128 v[98:101], v173 offset:6144
	v_lshl_add_u64 v[178:179], v[176:177], 0, s[34:35]
	v_mfma_f32_16x16x32_f16 v[22:25], v[168:171], v[160:163], v[22:25]
	s_cmp_lg_u32 s60, s66
	s_cbranch_scc1 .Lc3_nopatch
	s_ashr_i32 s36, s51, 31
	s_lshr_b32 s36, s36, 30
	s_add_i32 s36, s51, s36
	s_ashr_i32 s36, s36, 2
	s_mul_i32 s54, s36, 3
	s_add_i32 s54, s54, -1
	v_add_u32_e32 v140, s54, v126
	s_lshl_b32 s37, s51, 6
	s_lshl_b32 s36, s36, 8
	v_cmp_gt_u32_e32 vcc, 64, v140
	s_sub_i32 s53, s37, s36
	s_and_b64 s[36:37], s[2:3], vcc
	s_and_b64 s[56:57], s[36:37], s[4:5]
	v_mov_b64_e32 v[122:123], s[30:31]
	s_and_saveexec_b64 s[36:37], s[56:57]
	v_or_b32_e32 v122, s53, v140
	v_lshl_add_u32 v122, v122, 6, v127
	v_ashrrev_i32_e32 v123, 31, v122
	v_lshlrev_b64 v[122:123], 7, v[122:123]
	v_lshl_add_u64 v[122:123], v[120:121], 0, v[122:123]
	s_or_b64 exec, exec, s[36:37]
	s_bitcmp1_b32 s51, 0
	s_cselect_b32 s55, 0xc000, 0
	s_add_i32 s36, s55, s42
	v_add_u32_e32 v140, s36, v1
	s_nop 0
	v_readfirstlane_b32 s36, v140
	s_mov_b32 m0, s36
	v_add_u32_e32 v140, s54, v128
	global_load_lds_dwordx4 v[122:123], off
	v_cmp_gt_u32_e32 vcc, 64, v140
	s_and_b64 s[36:37], s[6:7], vcc
	s_and_b64 s[56:57], s[36:37], s[8:9]
	v_mov_b64_e32 v[122:123], s[30:31]
	s_and_saveexec_b64 s[36:37], s[56:57]
	v_or_b32_e32 v122, s53, v140
	v_lshl_add_u32 v122, v122, 6, v129
	v_ashrrev_i32_e32 v123, 31, v122
	v_lshlrev_b64 v[122:123], 7, v[122:123]
	v_lshl_add_u64 v[122:123], v[120:121], 0, v[122:123]
	s_or_b64 exec, exec, s[36:37]
	s_add_i32 s36, s55, s43
	v_add_u32_e32 v140, s36, v1
	s_nop 0
	v_readfirstlane_b32 s36, v140
	s_mov_b32 m0, s36
	v_add_u32_e32 v140, s54, v130
	global_load_lds_dwordx4 v[122:123], off
	v_cmp_gt_u32_e32 vcc, 64, v140
	s_and_b64 s[36:37], s[10:11], vcc
	s_and_b64 s[56:57], s[36:37], s[12:13]
	v_mov_b64_e32 v[122:123], s[30:31]
	s_and_saveexec_b64 s[36:37], s[56:57]
	v_or_b32_e32 v122, s53, v140
	v_lshl_add_u32 v122, v122, 6, v131
	v_ashrrev_i32_e32 v123, 31, v122
	v_lshlrev_b64 v[122:123], 7, v[122:123]
	v_lshl_add_u64 v[122:123], v[120:121], 0, v[122:123]
	s_or_b64 exec, exec, s[36:37]
	s_add_i32 s36, s55, s44
	v_add_u32_e32 v140, s36, v1
	s_nop 0
	v_readfirstlane_b32 s36, v140
	s_mov_b32 m0, s36
	v_add_u32_e32 v140, s54, v132
	global_load_lds_dwordx4 v[122:123], off
	v_cmp_gt_u32_e32 vcc, 64, v140
	s_and_b64 s[36:37], s[14:15], vcc
	s_and_b64 s[56:57], s[36:37], s[16:17]
	v_mov_b64_e32 v[122:123], s[30:31]
	s_and_saveexec_b64 s[36:37], s[56:57]
	v_or_b32_e32 v122, s53, v140
	v_lshl_add_u32 v122, v122, 6, v133
	v_ashrrev_i32_e32 v123, 31, v122
	v_lshlrev_b64 v[122:123], 7, v[122:123]
	v_lshl_add_u64 v[122:123], v[120:121], 0, v[122:123]
	s_or_b64 exec, exec, s[36:37]
	s_add_i32 s36, s55, s45
	v_add_u32_e32 v140, s36, v1
	s_nop 0
	v_readfirstlane_b32 s36, v140
	s_mov_b32 m0, s36
	v_add_u32_e32 v140, s54, v134
	global_load_lds_dwordx4 v[122:123], off
	v_cmp_gt_u32_e32 vcc, 64, v140
	s_and_b64 s[36:37], s[18:19], vcc
	s_and_b64 s[56:57], s[36:37], s[20:21]
	v_mov_b64_e32 v[122:123], s[30:31]
	s_and_saveexec_b64 s[36:37], s[56:57]
	v_or_b32_e32 v122, s53, v140
	v_lshl_add_u32 v122, v122, 6, v135
	v_ashrrev_i32_e32 v123, 31, v122
	v_lshlrev_b64 v[122:123], 7, v[122:123]
	v_lshl_add_u64 v[122:123], v[120:121], 0, v[122:123]
	s_or_b64 exec, exec, s[36:37]
	s_add_i32 s36, s55, s46
	v_add_u32_e32 v140, s36, v1
	s_nop 0
	v_readfirstlane_b32 s36, v140
	s_mov_b32 m0, s36
	v_add_u32_e32 v140, s54, v136
	global_load_lds_dwordx4 v[122:123], off
	v_cmp_gt_u32_e32 vcc, 64, v140
	s_and_b64 s[36:37], s[22:23], vcc
	s_and_b64 s[56:57], s[36:37], s[24:25]
	v_mov_b64_e32 v[122:123], s[30:31]
	s_and_saveexec_b64 s[36:37], s[56:57]
	s_cbranch_execz .Lc3_ptail
	v_or_b32_e32 v122, s53, v140
	v_lshl_add_u32 v122, v122, 6, v137
	v_ashrrev_i32_e32 v123, 31, v122
	v_lshlrev_b64 v[122:123], 7, v[122:123]
	v_lshl_add_u64 v[122:123], v[120:121], 0, v[122:123]
	s_branch .Lc3_ptail
.Lc3_ptail:
	s_or_b64 exec, exec, s[36:37]
	s_add_i32 s55, s55, s48
	v_add_u32_e32 v140, s55, v1
	s_add_i32 s51, s51, 1
	v_readfirstlane_b32 s36, v140
	s_mov_b32 m0, s36
	s_mov_b64 s[36:37], -1
	global_load_lds_dwordx4 v[122:123], off
	s_add_i32 s66, s66, 9
	s_cmp_gt_u32 s51, 3
	s_cselect_b32 s66, 0x3e8, s66
	s_mov_b32 s67, 2
.Lc3_nopatch:
	s_cmp_eq_u32 s60, 36
	s_cbranch_scc0 .Lc3_loop

	.amdhsa_kernel _Z6conv_kILi256ELi512ELi3ELi128ELi1ELi1ELb0EEvPKDF16_S1_PKfS3_PDF16_S4_S1_fS3_S3_S3_S3_
		.amdhsa_group_segment_fixed_size 163840
		.amdhsa_private_segment_fixed_size 0
		.amdhsa_kernarg_size 96
		.amdhsa_user_sgpr_count 2
		.amdhsa_user_sgpr_dispatch_ptr 0
		.amdhsa_user_sgpr_queue_ptr 0
		.amdhsa_user_sgpr_kernarg_segment_ptr 1
		.amdhsa_user_sgpr_dispatch_id 0
		.amdhsa_user_sgpr_kernarg_preload_length 0
		.amdhsa_user_sgpr_kernarg_preload_offset 0
		.amdhsa_user_sgpr_private_segment_size 0
		.amdhsa_uses_dynamic_stack 0
		.amdhsa_enable_private_segment 0
		.amdhsa_system_sgpr_workgroup_id_x 1
		.amdhsa_system_sgpr_workgroup_id_y 0
		.amdhsa_system_sgpr_workgroup_id_z 0
		.amdhsa_system_sgpr_workgroup_info 0
		.amdhsa_system_vgpr_workitem_id 0
		.amdhsa_next_free_vgpr 184
		.amdhsa_next_free_sgpr 96
		.amdhsa_accum_offset 184
		.amdhsa_reserve_vcc 1
		.amdhsa_float_round_mode_32 0
		.amdhsa_float_round_mode_16_64 0
		.amdhsa_float_denorm_mode_32 3
		.amdhsa_float_denorm_mode_16_64 3
		.amdhsa_dx10_clamp 1
		.amdhsa_ieee_mode 1
		.amdhsa_fp16_overflow 0
		.amdhsa_tg_split 0
		.amdhsa_exception_fp_ieee_invalid_op 0
		.amdhsa_exception_fp_denorm_src 0
		.amdhsa_exception_fp_ieee_div_zero 0
		.amdhsa_exception_fp_ieee_overflow 0
		.amdhsa_exception_fp_ieee_underflow 0
		.amdhsa_exception_fp_ieee_inexact 0
		.amdhsa_exception_int_div_zero 0
	.end_amdhsa_kernel

_Z6conv_kILi512ELi256ELi3ELi64ELi1ELi1ELb0EEvPKDF16_S1_PKfS3_PDF16_S4_S1_fS3_S3_S3_S3_:
	s_lshl_b32 s3, s2, 3
	s_load_dwordx2 s[36:37], s[0:1], 0x0
	s_load_dwordx4 s[4:7], s[0:1], 0x10
	s_load_dwordx2 s[30:31], s[0:1], 0x30
	s_and_b32 s3, s3, 56
	s_ashr_i32 s8, s2, 5
	s_add_i32 s3, s3, s8
	v_readfirstlane_b32 s42, v0
	s_lshl_b32 s8, s3, 2
	s_bfe_u32 s38, s2, 0x20003
	s_and_b32 s33, s8, 56
	s_lshr_b32 s52, s42, 6
	s_ashr_i32 s40, s3, 4
	s_and_b32 s27, s2, 32
	s_lshl_b32 s2, s38, 8
	v_bfe_u32 v29, v0, 3, 3
	v_and_b32_e32 v2, 7, v0
	s_waitcnt lgkmcnt(0)
	s_add_u32 s2, s4, s2
	v_bitop3_b32 v2, v29, v2, 6 bitop3:0x6c
	s_addc_u32 s3, s5, 0
	v_and_b32_e32 v18, 48, v0
	v_mov_b32_e32 v19, 0
	v_lshlrev_b32_e32 v20, 3, v2
	v_lshl_add_u64 v[2:3], s[2:3], 0, v[18:19]
	s_load_dword s26, s[6:7], 0x0
	global_load_dwordx4 v[14:17], v[2:3], off
	v_lshl_add_u64 v[4:5], v[2:3], 0, 64
	s_mov_b64 s[2:3], 0x80
	global_load_dwordx4 v[10:13], v[4:5], off
	v_lshl_add_u64 v[4:5], v[2:3], 0, s[2:3]
	s_mov_b64 s[2:3], 0xc0
	v_lshl_add_u64 v[2:3], v[2:3], 0, s[2:3]
	v_lshl_or_b32 v18, s52, 3, v29
	s_mov_b32 s2, 0x1e1e1e1f
	v_mul_hi_u32 v21, v18, s2
	v_lshrrev_b32_e32 v21, 2, v21
	s_movk_i32 s8, 0xffde
	s_add_i32 s24, s33, -1
	global_load_dwordx4 v[6:9], v[4:5], off
	v_mul_lo_u32 v22, v21, s8
	v_add_u32_e32 v25, s24, v21
	s_add_i32 s25, s27, -1
	s_movk_i32 s9, 0x154
	global_load_dwordx4 v[2:5], v[2:3], off
	v_add3_u32 v24, s25, v18, v22
	v_cmp_gt_u32_e64 s[2:3], s9, v18
	v_cmp_gt_u32_e32 vcc, 64, v25
	s_and_b64 s[6:7], s[2:3], vcc
	v_cmp_gt_u32_e64 s[4:5], 64, v24
	v_and_b32_e32 v1, 63, v0
	s_and_b64 s[10:11], s[6:7], s[4:5]
	v_mov_b64_e32 v[22:23], s[30:31]
	v_lshlrev_b32_e32 v18, 1, v20
	s_and_saveexec_b64 s[6:7], s[10:11]
	s_lshl_b32 s10, s40, 15
	v_lshlrev_b32_e32 v22, 6, v25
	v_or3_b32 v22, v22, s10, v24
	v_ashrrev_i32_e32 v23, 31, v22
	v_lshlrev_b64 v[22:23], 7, v[22:23]
	v_lshl_add_u64 v[22:23], s[36:37], 0, v[22:23]
	v_lshl_add_u64 v[22:23], v[22:23], 0, v[18:19]
	s_or_b64 exec, exec, s[6:7]
	s_lshl_b32 s43, s52, 10
	v_lshlrev_b32_e32 v120, 4, v1
	v_or_b32_e32 v19, s43, v120
	s_add_i32 s13, s52, 8
	v_readfirstlane_b32 s6, v19
	s_mov_b32 m0, s6
	s_mov_b32 s12, 0x3c3c3c3d
	global_load_lds_dwordx4 v[22:23], off
	v_lshl_or_b32 v22, s13, 3, v29
	v_mul_hi_u32 v19, v22, s12
	v_lshrrev_b32_e32 v25, 3, v19
	v_mul_lo_u32 v23, v25, s8
	v_add_u32_e32 v19, s24, v25
	v_add3_u32 v26, s25, v22, v23
	v_cmp_gt_u32_e64 s[6:7], s9, v22
	v_cmp_gt_u32_e32 vcc, 64, v19
	s_and_b64 s[10:11], s[6:7], vcc
	v_cmp_gt_u32_e64 s[8:9], 64, v26
	s_and_b64 s[14:15], s[10:11], s[8:9]
	v_mov_b64_e32 v[22:23], s[30:31]
	s_and_saveexec_b64 s[10:11], s[14:15]
	s_lshl_b32 s14, s40, 15
	v_lshlrev_b32_e32 v19, 6, v19
	v_or3_b32 v22, v19, s14, v26
	v_ashrrev_i32_e32 v23, 31, v22
	v_lshlrev_b64 v[22:23], 7, v[22:23]
	v_lshl_add_u64 v[22:23], s[36:37], 0, v[22:23]
	v_mov_b32_e32 v19, 0
	v_lshl_add_u64 v[22:23], v[22:23], 0, v[18:19]
	s_or_b64 exec, exec, s[10:11]
	s_lshl_b32 s44, s13, 10
	v_or_b32_e32 v19, s44, v120
	s_add_i32 s18, s52, 16
	v_readfirstlane_b32 s10, v19
	s_mov_b32 m0, s10
	s_movk_i32 s16, 0xffde
	global_load_lds_dwordx4 v[22:23], off
	v_lshl_or_b32 v22, s18, 3, v29
	v_mul_hi_u32 v19, v22, s12
	v_lshrrev_b32_e32 v27, 3, v19
	v_mul_lo_u32 v23, v27, s16
	v_add_u32_e32 v19, s24, v27
	s_movk_i32 s17, 0x154
	v_add3_u32 v28, s25, v22, v23
	v_cmp_gt_u32_e64 s[10:11], s17, v22
	v_cmp_gt_u32_e32 vcc, 64, v19
	s_and_b64 s[14:15], s[10:11], vcc
	v_cmp_gt_u32_e64 s[12:13], 64, v28
	s_and_b64 s[20:21], s[14:15], s[12:13]
	v_mov_b64_e32 v[22:23], s[30:31]
	s_and_saveexec_b64 s[14:15], s[20:21]
	s_lshl_b32 s19, s40, 15
	v_lshlrev_b32_e32 v19, 6, v19
	v_or3_b32 v22, v19, s19, v28
	v_ashrrev_i32_e32 v23, 31, v22
	v_lshlrev_b64 v[22:23], 7, v[22:23]
	v_lshl_add_u64 v[22:23], s[36:37], 0, v[22:23]
	v_mov_b32_e32 v19, 0
	v_lshl_add_u64 v[22:23], v[22:23], 0, v[18:19]
	s_or_b64 exec, exec, s[14:15]
	s_lshl_b32 s45, s18, 10
	v_or_b32_e32 v19, s45, v120
	s_add_i32 s21, s52, 24
	v_readfirstlane_b32 s14, v19
	s_mov_b32 m0, s14
	s_mov_b32 s20, 0x3c3c3c3d
	global_load_lds_dwordx4 v[22:23], off
	v_lshl_or_b32 v22, s21, 3, v29
	v_mul_hi_u32 v19, v22, s20
	v_lshrrev_b32_e32 v30, 3, v19
	v_mul_lo_u32 v23, v30, s16
	v_add_u32_e32 v19, s24, v30
	v_add3_u32 v31, s25, v22, v23
	v_cmp_gt_u32_e64 s[14:15], s17, v22
	v_cmp_gt_u32_e32 vcc, 64, v19
	s_and_b64 s[18:19], s[14:15], vcc
	v_cmp_gt_u32_e64 s[16:17], 64, v31
	s_and_b64 s[22:23], s[18:19], s[16:17]
	v_mov_b64_e32 v[22:23], s[30:31]
	s_and_saveexec_b64 s[18:19], s[22:23]
	s_lshl_b32 s22, s40, 15
	v_lshlrev_b32_e32 v19, 6, v19
	v_or3_b32 v22, v19, s22, v31
	v_ashrrev_i32_e32 v23, 31, v22
	v_lshlrev_b64 v[22:23], 7, v[22:23]
	v_lshl_add_u64 v[22:23], s[36:37], 0, v[22:23]
	v_mov_b32_e32 v19, 0
	v_lshl_add_u64 v[22:23], v[22:23], 0, v[18:19]
	s_or_b64 exec, exec, s[18:19]
	s_lshl_b32 s46, s21, 10
	v_or_b32_e32 v19, s46, v120
	s_add_i32 s28, s52, 32
	v_readfirstlane_b32 s18, v19
	s_mov_b32 m0, s18
	s_movk_i32 s18, 0xffde
	global_load_lds_dwordx4 v[22:23], off
	v_lshl_or_b32 v22, s28, 3, v29
	v_mul_hi_u32 v19, v22, s20
	v_lshrrev_b32_e32 v32, 3, v19
	v_mul_lo_u32 v23, v32, s18
	v_add_u32_e32 v19, s24, v32
	s_movk_i32 s18, 0x154
	v_add3_u32 v33, s25, v22, v23
	v_cmp_gt_u32_e64 s[18:19], s18, v22
	v_cmp_gt_u32_e32 vcc, 64, v19
	s_and_b64 s[22:23], s[18:19], vcc
	v_cmp_gt_u32_e64 s[20:21], 64, v33
	s_and_b64 s[22:23], s[22:23], s[20:21]
	s_xor_b64 s[22:23], s[22:23], -1
	s_and_saveexec_b64 s[34:35], s[22:23]
	s_xor_b64 s[22:23], exec, s[34:35]
	s_lshl_b32 s29, s40, 15
	s_or_saveexec_b64 s[22:23], s[22:23]
	v_mov_b32_e32 v34, s29
	v_mov_b64_e32 v[22:23], s[30:31]
	s_xor_b64 exec, exec, s[22:23]
	s_lshl_b32 s29, s40, 15
	v_lshlrev_b32_e32 v19, 6, v19
	v_or3_b32 v22, v19, s29, v33
	v_ashrrev_i32_e32 v23, 31, v22
	v_lshlrev_b64 v[22:23], 7, v[22:23]
	v_lshl_add_u64 v[22:23], s[36:37], 0, v[22:23]
	v_mov_b32_e32 v19, 0
	v_lshl_add_u64 v[22:23], v[22:23], 0, v[18:19]
	v_mov_b32_e32 v34, s29
	s_or_b64 exec, exec, s[22:23]
	s_lshl_b32 s47, s28, 10
	v_or_b32_e32 v18, s47, v120
	s_add_i32 s39, s52, 40
	v_readfirstlane_b32 s22, v18
	s_mov_b32 m0, s22
	v_lshl_or_b32 v18, s39, 3, v29
	global_load_lds_dwordx4 v[22:23], off
	s_mov_b32 s22, 0x3c3c3c3d
	v_mul_hi_u32 v19, v18, s22
	v_lshrrev_b32_e32 v22, 3, v19
	s_movk_i32 s22, 0xffde
	s_load_dwordx2 s[34:35], s[0:1], 0x8
	v_mul_lo_u32 v19, v22, s22
	v_add_u32_e32 v35, s24, v22
	s_movk_i32 s22, 0x154
	v_add3_u32 v23, s25, v18, v19
	v_cmp_gt_u32_e64 s[22:23], s22, v18
	v_cmp_gt_u32_e32 vcc, 64, v35
	s_and_b64 s[28:29], s[22:23], vcc
	v_cmp_gt_u32_e64 s[24:25], 64, v23
	s_and_b64 s[28:29], s[28:29], s[24:25]
	s_xor_b64 s[28:29], s[28:29], -1
	s_and_saveexec_b64 s[48:49], s[28:29]
	s_xor_b64 s[28:29], exec, s[48:49]
	s_or_saveexec_b64 s[28:29], s[28:29]
	v_mov_b64_e32 v[18:19], s[30:31]
	s_xor_b64 exec, exec, s[28:29]
	v_lshlrev_b32_e32 v18, 6, v35
	v_or3_b32 v18, v18, v34, v23
	v_ashrrev_i32_e32 v19, 31, v18
	v_lshlrev_b64 v[18:19], 7, v[18:19]
	v_lshl_add_u64 v[18:19], s[36:37], 0, v[18:19]
	v_lshlrev_b32_e32 v36, 1, v20
	v_mov_b32_e32 v37, 0
	v_lshl_add_u64 v[18:19], v[18:19], 0, v[36:37]
	s_or_b64 exec, exec, s[28:29]
	v_lshrrev_b32_e32 v122, 4, v1
	v_bitop3_b32 v35, v122, v0, 6 bitop3:0x78
	s_and_b32 s48, s52, 3
	v_lshl_or_b32 v29, v29, 6, s43
	s_movk_i32 s50, 0xdc0
	v_and_b32_e32 v121, 15, v0
	v_lshlrev_b32_e32 v35, 4, v35
	s_lshr_b32 s49, s42, 8
	v_and_or_b32 v29, v29, s50, v20
	s_mul_i32 s50, s48, 0x44
	v_lshl_or_b32 v35, v121, 7, v35
	v_add_u32_e32 v123, s50, v121
	v_lshl_or_b32 v35, s49, 13, v35
	s_lshl_b32 s50, s39, 10
	s_lshl_b32 s41, s38, 6
	v_add_u32_e32 v125, 0x18000, v35
	v_or_b32_e32 v35, s50, v120
	s_lshl_b32 s38, s38, 13
	v_readfirstlane_b32 s39, v35
	s_waitcnt lgkmcnt(0)
	s_add_u32 s38, s34, s38
	s_mul_hi_u32 s57, s42, 0x38e38e39
	s_mov_b32 m0, s39
	s_addc_u32 s39, s35, 0
	s_lshr_b32 s34, s57, 12
	s_mulk_i32 s34, 0xffc1
	s_add_i32 s34, s34, s49
	s_lshl_b32 s56, s52, 11
	s_ashr_i32 s35, s34, 31
	s_add_i32 s52, s56, 0x18000
	s_lshl_b64 s[34:35], s[34:35], 15
	s_add_u32 s34, s38, s34
	s_addc_u32 s35, s39, s35
	s_add_i32 s54, s49, 2
	s_mul_hi_u32 s55, s54, 0x38e38e4
	s_mulk_i32 s55, 0xffc1
	s_add_i32 s54, s55, s54
	global_load_lds_dwordx4 v[18:19], off
	v_lshlrev_b32_e32 v18, 1, v29
	v_mov_b32_e32 v19, 0
	s_mov_b32 m0, s52
	s_ashr_i32 s55, s54, 31
	v_lshl_add_u64 v[36:37], s[34:35], 0, v[18:19]
	global_load_lds_dwordx4 v18, s[34:35]
	s_mov_b64 s[34:35], 0x400
	s_add_i32 m0, s56, 0x18400
	s_lshl_b64 s[54:55], s[54:55], 15
	v_lshl_add_u64 v[36:37], v[36:37], 0, s[34:35]
	s_add_u32 s54, s38, s54
	global_load_lds_dwordx4 v[36:37], off
	s_addc_u32 s55, s39, s55
	s_add_i32 m0, s56, 0x1c000
	v_lshl_add_u64 v[36:37], s[54:55], 0, v[18:19]
	global_load_lds_dwordx4 v18, s[54:55]
	s_add_i32 s54, s49, 4
	s_mul_hi_u32 s55, s54, 0x38e38e4
	s_mulk_i32 s55, 0xffc1
	s_add_i32 s54, s55, s54
	s_ashr_i32 s55, s54, 31
	s_add_i32 m0, s56, 0x1c400
	s_lshl_b64 s[54:55], s[54:55], 15
	s_add_u32 s54, s38, s54
	v_lshl_add_u64 v[36:37], v[36:37], 0, s[34:35]
	s_addc_u32 s55, s39, s55
	global_load_lds_dwordx4 v[36:37], off
	s_add_i32 m0, s56, 0x20000
	v_lshl_add_u64 v[36:37], s[54:55], 0, v[18:19]
	global_load_lds_dwordx4 v18, s[54:55]
	v_lshl_add_u64 v[36:37], v[36:37], 0, s[34:35]
	s_add_i32 m0, s56, 0x20400
	s_lshr_b32 s54, s57, 9
	global_load_lds_dwordx4 v[36:37], off
	s_mul_i32 s54, s54, -9
	s_add_i32 s54, s54, s49
	s_mul_hi_i32 s55, s54, 0x55555556
	s_lshr_b32 s56, s55, 31
	s_add_i32 s55, s55, s56
	s_mul_i32 s55, s55, 31
	s_add_i32 s55, s55, s54
	s_bitcmp1_b32 s57, 9
	s_waitcnt vmcnt(4) lgkmcnt(0)
	s_barrier
	s_cselect_b32 s54, 0xc000, 0
	ds_read_b128 v[62:65], v125
	v_add_u32_e32 v29, s55, v123
	v_add_u32_e32 v124, 34, v123
	ds_read_b128 v[58:61], v125 offset:2048
	v_bitop3_b32 v35, v29, v122, 6 bitop3:0x6c
	v_lshl_add_u32 v29, v29, 7, s54
	v_lshl_or_b32 v139, v35, 4, v29
	ds_read_b128 v[70:73], v139
	v_add_u32_e32 v29, s55, v124
	ds_read_b128 v[66:69], v139 offset:2048
	v_bitop3_b32 v35, v29, v122, 6 bitop3:0x6c
	v_lshl_add_u32 v29, v29, 7, s54
	v_lshl_or_b32 v140, v35, 4, v29
	ds_read_b128 v[82:85], v140
	s_load_dwordx2 s[28:29], s[0:1], 0x20
	ds_read_b128 v[78:81], v140 offset:2048
	ds_read_b128 v[90:93], v125 offset:4096
	ds_read_b128 v[86:89], v125 offset:6144
	v_add_u32_e32 v127, s33, v21
	v_lshlrev_b32_e32 v20, 1, v20
	v_mov_b32_e32 v21, v19
	v_xor_b32_e32 v126, 64, v125
	s_mov_b32 s51, 0
	s_mov_b32 s53, 1
	v_add_u32_e32 v128, v34, v24
	v_lshl_add_u64 v[114:115], s[36:37], 0, v[20:21]
	v_add_u32_e32 v129, s33, v25
	v_add_u32_e32 v130, v34, v26
	v_add_u32_e32 v131, s33, v27
	v_add_u32_e32 v132, v34, v28
	v_add_u32_e32 v133, s33, v30
	v_add_u32_e32 v134, v34, v31
	v_add_u32_e32 v135, s33, v32
	v_add_u32_e32 v136, v34, v33
	v_add_u32_e32 v137, s33, v22
	v_add_u32_e32 v138, v34, v23
	v_lshl_add_u64 v[116:117], s[38:39], 0, v[18:19]
	s_mov_b64 s[36:37], 0
	s_mov_b32 s38, 0
	s_mov_b32 s39, 0
	v_mov_b32_e32 v18, v19
	v_mov_b32_e32 v20, v19
	v_mov_b32_e32 v22, v19
	v_mov_b32_e32 v23, v19
	v_mov_b32_e32 v24, v19
	v_mov_b32_e32 v25, v19
	v_mov_b32_e32 v26, v19
	v_mov_b32_e32 v27, v19
	v_mov_b32_e32 v28, v19
	v_mov_b32_e32 v29, v19
	v_mov_b32_e32 v42, v19
	v_mov_b32_e32 v43, v19
	v_mov_b32_e32 v44, v19
	v_mov_b32_e32 v45, v19
	v_mov_b32_e32 v50, v19
	v_mov_b32_e32 v51, v19
	v_mov_b32_e32 v52, v19
	v_mov_b32_e32 v53, v19
	v_mov_b32_e32 v54, v19
	v_mov_b32_e32 v55, v19
	v_mov_b32_e32 v56, v19
	v_mov_b32_e32 v57, v19
	v_mov_b32_e32 v74, v19
	v_mov_b32_e32 v75, v19
	v_mov_b32_e32 v76, v19
	v_mov_b32_e32 v77, v19
	v_mov_b32_e32 v94, v19
	v_mov_b32_e32 v95, v19
	v_mov_b32_e32 v96, v19
	v_mov_b32_e32 v97, v19
	v_mov_b32_e32 v98, v19
	v_mov_b32_e32 v99, v19
	v_mov_b32_e32 v100, v19
	v_mov_b32_e32 v101, v19
	v_mov_b32_e32 v102, v19
	v_mov_b32_e32 v103, v19
	v_mov_b32_e32 v104, v19
	v_mov_b32_e32 v105, v19
	v_mov_b32_e32 v106, v19
	v_mov_b32_e32 v107, v19
	v_mov_b32_e32 v108, v19
	v_mov_b32_e32 v109, v19
	v_mov_b32_e32 v110, v19
	v_mov_b32_e32 v111, v19
	v_mov_b32_e32 v112, v19
	v_mov_b32_e32 v113, v19
	v_mov_b32_e32 v46, v19
	v_mov_b32_e32 v47, v19
	v_mov_b32_e32 v48, v19
	v_mov_b32_e32 v49, v19
	v_mov_b32_e32 v30, v19
	v_mov_b32_e32 v31, v19
	v_mov_b32_e32 v32, v19
	v_mov_b32_e32 v33, v19
	v_mov_b32_e32 v38, v19
	v_mov_b32_e32 v39, v19
	v_mov_b32_e32 v40, v19
	v_mov_b32_e32 v41, v19
	v_mov_b32_e32 v34, v19
	v_mov_b32_e32 v35, v19
	v_mov_b32_e32 v36, v19
	v_mov_b32_e32 v37, v19
	s_mov_b32 s60, 0
	s_add_i32 s63, s49, 2
	s_mul_i32 s73, s63, 11
	s_lshr_b32 s73, s73, 5
	s_mul_i32 s73, s73, 31
	s_add_i32 s62, s63, s73
	s_mov_b32 s64, 0
	s_mov_b32 s66, 1
	s_mov_b32 s67, 0
	s_add_i32 s75, s49, 6
	s_lshl_b32 s68, s75, 15
	s_mov_b32 s69, 0
	v_lshl_add_u64 v[178:179], v[116:117], 0, s[68:69]
	s_add_i32 s70, s52, 0xc000
	v_lshl_add_u64 v[180:181], v[178:179], 0, s[34:35]
	v_mov_b32_e32 v174, v126

.Lc4_bar:
	s_barrier
	s_waitcnt lgkmcnt(5)
	v_mfma_f32_16x16x32_f16 v[110:113], v[62:65], v[70:73], v[110:113]
	ds_read_b128 v[142:145], v174
	v_mfma_f32_16x16x32_f16 v[106:109], v[58:61], v[70:73], v[106:109]
	v_xor_b32_e32 v176, 64, v139
	s_waitcnt lgkmcnt(5)
	v_mfma_f32_16x16x32_f16 v[94:97], v[62:65], v[66:69], v[94:97]
	ds_read_b128 v[146:149], v174 offset:2048
	v_mfma_f32_16x16x32_f16 v[74:77], v[58:61], v[66:69], v[74:77]
	v_xor_b32_e32 v177, 64, v140
	s_mov_b32 m0, s70
	s_add_i32 s71, s38, 0x4000
	global_load_lds_dwordx4 v[178:179], off
	s_waitcnt lgkmcnt(5)
	v_mfma_f32_16x16x32_f16 v[42:45], v[62:65], v[82:85], v[42:45]
	ds_read_b128 v[150:153], v176
	v_mfma_f32_16x16x32_f16 v[26:29], v[58:61], v[82:85], v[26:29]
	s_and_b32 s71, s71, 0xc000
	s_add_i32 s72, s70, 0x400
	s_waitcnt lgkmcnt(5)
	v_mfma_f32_16x16x32_f16 v[46:49], v[62:65], v[78:81], v[46:49]
	ds_read_b128 v[154:157], v176 offset:2048
	v_mfma_f32_16x16x32_f16 v[30:33], v[58:61], v[78:81], v[30:33]
	v_add_u32_e32 v175, s71, v125
	s_waitcnt lgkmcnt(5)
	v_mfma_f32_16x16x32_f16 v[102:105], v[90:93], v[70:73], v[102:105]
	ds_read_b128 v[158:161], v177
	s_waitcnt lgkmcnt(5)
	v_mfma_f32_16x16x32_f16 v[98:101], v[86:89], v[70:73], v[98:101]
	v_mfma_f32_16x16x32_f16 v[54:57], v[90:93], v[66:69], v[54:57]
	ds_read_b128 v[162:165], v177 offset:2048
	v_mfma_f32_16x16x32_f16 v[50:53], v[86:89], v[66:69], v[50:53]
	v_add_u32_e32 v182, s62, v123
	v_mfma_f32_16x16x32_f16 v[22:25], v[90:93], v[82:85], v[22:25]
	ds_read_b128 v[166:169], v174 offset:4096
	v_mfma_f32_16x16x32_f16 v[18:21], v[86:89], v[82:85], v[18:21]
	v_bitop3_b32 v183, v182, v122, 6 bitop3:0x6c
	v_lshl_add_u32 v182, v182, 7, s64
	v_mfma_f32_16x16x32_f16 v[38:41], v[90:93], v[78:81], v[38:41]
	ds_read_b128 v[170:173], v174 offset:6144
	v_mfma_f32_16x16x32_f16 v[34:37], v[86:89], v[78:81], v[34:37]
	v_lshl_or_b32 v139, v183, 4, v182
	v_add_u32_e32 v174, s71, v126
	s_waitcnt lgkmcnt(5)
	v_mfma_f32_16x16x32_f16 v[110:113], v[142:145], v[150:153], v[110:113]
	ds_read_b128 v[62:65], v175
	v_mfma_f32_16x16x32_f16 v[106:109], v[146:149], v[150:153], v[106:109]
	s_mov_b32 m0, s72
	s_add_i32 s63, s63, 2
	global_load_lds_dwordx4 v[180:181], off
	s_waitcnt lgkmcnt(5)
	v_mfma_f32_16x16x32_f16 v[94:97], v[142:145], v[154:157], v[94:97]
	ds_read_b128 v[58:61], v175 offset:2048
	v_mfma_f32_16x16x32_f16 v[74:77], v[146:149], v[154:157], v[74:77]
	v_add_u32_e32 v182, s62, v124
	s_waitcnt lgkmcnt(5)
	v_mfma_f32_16x16x32_f16 v[42:45], v[142:145], v[158:161], v[42:45]
	ds_read_b128 v[70:73], v139
	v_mfma_f32_16x16x32_f16 v[26:29], v[146:149], v[158:161], v[26:29]
	v_bitop3_b32 v183, v182, v122, 6 bitop3:0x6c
	v_lshl_add_u32 v182, v182, 7, s64
	s_waitcnt lgkmcnt(5)
	v_mfma_f32_16x16x32_f16 v[46:49], v[142:145], v[162:165], v[46:49]
	ds_read_b128 v[66:69], v139 offset:2048
	v_mfma_f32_16x16x32_f16 v[30:33], v[146:149], v[162:165], v[30:33]
	v_lshl_or_b32 v140, v183, 4, v182
	s_waitcnt lgkmcnt(5)
	v_mfma_f32_16x16x32_f16 v[102:105], v[166:169], v[150:153], v[102:105]
	ds_read_b128 v[82:85], v140
	s_waitcnt lgkmcnt(5)
	v_mfma_f32_16x16x32_f16 v[98:101], v[170:173], v[150:153], v[98:101]
	s_cmp_ge_u32 s63, 9
	s_cselect_b32 s73, 9, 0
	s_cselect_b32 s74, 0xc000, 0
	s_sub_i32 s63, s63, s73
	s_xor_b32 s64, s64, s74
	v_mfma_f32_16x16x32_f16 v[54:57], v[166:169], v[154:157], v[54:57]
	ds_read_b128 v[78:81], v140 offset:2048
	s_mul_i32 s73, s63, 11
	s_lshr_b32 s73, s73, 5
	s_mul_i32 s73, s73, 31
	s_add_i32 s62, s63, s73
	v_mfma_f32_16x16x32_f16 v[50:53], v[170:173], v[154:157], v[50:53]
	s_addk_i32 s38, 0x4000
	s_add_i32 s60, s60, 1
	s_add_i32 s75, s60, 3
	s_cmp_lt_u32 s60, 33
	s_cselect_b32 s75, s75, 35
	s_lshl_b32 s75, s75, 1
	s_add_i32 s75, s75, s49
	s_lshl_b32 s68, s75, 15
	v_mfma_f32_16x16x32_f16 v[22:25], v[166:169], v[158:161], v[22:25]
	ds_read_b128 v[90:93], v175 offset:4096
	v_mfma_f32_16x16x32_f16 v[18:21], v[170:173], v[158:161], v[18:21]
	v_lshl_add_u64 v[178:179], v[116:117], 0, s[68:69]
	s_add_i32 s70, s38, 0xc000
	s_and_b32 s70, s70, 0xc000
	s_add_i32 s70, s70, s52
	v_mfma_f32_16x16x32_f16 v[38:41], v[166:169], v[162:165], v[38:41]
	ds_read_b128 v[86:89], v175 offset:6144
	v_lshl_add_u64 v[180:181], v[178:179], 0, s[34:35]
	v_mfma_f32_16x16x32_f16 v[34:37], v[170:173], v[162:165], v[34:37]
	s_cmp_lg_u32 s60, s66
	s_cbranch_scc1 .Lc4_nopatch
	s_ashr_i32 s36, s53, 31
	s_lshr_b32 s36, s36, 29
	s_add_i32 s36, s53, s36
	s_ashr_i32 s36, s36, 3
	s_mul_i32 s55, s36, 3
	s_add_i32 s55, s55, -1
	v_add_u32_e32 v141, s55, v127
	s_lshl_b32 s37, s53, 6
	s_lshl_b32 s36, s36, 9
	v_cmp_gt_u32_e32 vcc, 64, v141
	s_sub_i32 s54, s37, s36
	s_and_b64 s[36:37], s[2:3], vcc
	s_and_b64 s[56:57], s[36:37], s[4:5]
	v_mov_b64_e32 v[118:119], s[30:31]
	s_and_saveexec_b64 s[36:37], s[56:57]
	v_or_b32_e32 v118, s54, v141
	v_lshl_add_u32 v118, v118, 6, v128
	v_ashrrev_i32_e32 v119, 31, v118
	v_lshlrev_b64 v[118:119], 7, v[118:119]
	v_lshl_add_u64 v[118:119], v[114:115], 0, v[118:119]
	s_or_b64 exec, exec, s[36:37]
	s_bitcmp1_b32 s53, 0
	s_cselect_b32 s56, 0xc000, 0
	s_add_i32 s36, s56, s43
	v_add_u32_e32 v141, s36, v120
	s_nop 0
	v_readfirstlane_b32 s36, v141
	s_mov_b32 m0, s36
	v_add_u32_e32 v141, s55, v129
	global_load_lds_dwordx4 v[118:119], off
	v_cmp_gt_u32_e32 vcc, 64, v141
	s_and_b64 s[36:37], s[6:7], vcc
	s_and_b64 s[58:59], s[36:37], s[8:9]
	v_mov_b64_e32 v[118:119], s[30:31]
	s_and_saveexec_b64 s[36:37], s[58:59]
	v_or_b32_e32 v118, s54, v141
	v_lshl_add_u32 v118, v118, 6, v130
	v_ashrrev_i32_e32 v119, 31, v118
	v_lshlrev_b64 v[118:119], 7, v[118:119]
	v_lshl_add_u64 v[118:119], v[114:115], 0, v[118:119]
	s_or_b64 exec, exec, s[36:37]
	s_add_i32 s36, s56, s44
	v_add_u32_e32 v141, s36, v120
	s_nop 0
	v_readfirstlane_b32 s36, v141
	s_mov_b32 m0, s36
	v_add_u32_e32 v141, s55, v131
	global_load_lds_dwordx4 v[118:119], off
	v_cmp_gt_u32_e32 vcc, 64, v141
	s_and_b64 s[36:37], s[10:11], vcc
	s_and_b64 s[58:59], s[36:37], s[12:13]
	v_mov_b64_e32 v[118:119], s[30:31]
	s_and_saveexec_b64 s[36:37], s[58:59]
	v_or_b32_e32 v118, s54, v141
	v_lshl_add_u32 v118, v118, 6, v132
	v_ashrrev_i32_e32 v119, 31, v118
	v_lshlrev_b64 v[118:119], 7, v[118:119]
	v_lshl_add_u64 v[118:119], v[114:115], 0, v[118:119]
	s_or_b64 exec, exec, s[36:37]
	s_add_i32 s36, s56, s45
	v_add_u32_e32 v141, s36, v120
	s_nop 0
	v_readfirstlane_b32 s36, v141
	s_mov_b32 m0, s36
	v_add_u32_e32 v141, s55, v133
	global_load_lds_dwordx4 v[118:119], off
	v_cmp_gt_u32_e32 vcc, 64, v141
	s_and_b64 s[36:37], s[14:15], vcc
	s_and_b64 s[58:59], s[36:37], s[16:17]
	v_mov_b64_e32 v[118:119], s[30:31]
	s_and_saveexec_b64 s[36:37], s[58:59]
	v_or_b32_e32 v118, s54, v141
	v_lshl_add_u32 v118, v118, 6, v134
	v_ashrrev_i32_e32 v119, 31, v118
	v_lshlrev_b64 v[118:119], 7, v[118:119]
	v_lshl_add_u64 v[118:119], v[114:115], 0, v[118:119]
	s_or_b64 exec, exec, s[36:37]
	s_add_i32 s36, s56, s46
	v_add_u32_e32 v141, s36, v120
	s_nop 0
	v_readfirstlane_b32 s36, v141
	s_mov_b32 m0, s36
	v_add_u32_e32 v141, s55, v135
	global_load_lds_dwordx4 v[118:119], off
	v_cmp_gt_u32_e32 vcc, 64, v141
	s_and_b64 s[36:37], s[18:19], vcc
	s_and_b64 s[58:59], s[36:37], s[20:21]
	v_mov_b64_e32 v[118:119], s[30:31]
	s_and_saveexec_b64 s[36:37], s[58:59]
	v_or_b32_e32 v118, s54, v141
	v_lshl_add_u32 v118, v118, 6, v136
	v_ashrrev_i32_e32 v119, 31, v118
	v_lshlrev_b64 v[118:119], 7, v[118:119]
	v_lshl_add_u64 v[118:119], v[114:115], 0, v[118:119]
	s_or_b64 exec, exec, s[36:37]
	s_add_i32 s36, s56, s47
	v_add_u32_e32 v141, s36, v120
	s_nop 0
	v_readfirstlane_b32 s36, v141
	s_mov_b32 m0, s36
	v_add_u32_e32 v141, s55, v137
	global_load_lds_dwordx4 v[118:119], off
	v_cmp_gt_u32_e32 vcc, 64, v141
	s_and_b64 s[36:37], s[22:23], vcc
	s_and_b64 s[58:59], s[36:37], s[24:25]
	v_mov_b64_e32 v[118:119], s[30:31]
	s_and_saveexec_b64 s[36:37], s[58:59]
	s_cbranch_execz .Lc4_ptail
	v_or_b32_e32 v118, s54, v141
	v_lshl_add_u32 v118, v118, 6, v138
	v_ashrrev_i32_e32 v119, 31, v118
	v_lshlrev_b64 v[118:119], 7, v[118:119]
	v_lshl_add_u64 v[118:119], v[114:115], 0, v[118:119]
	s_branch .Lc4_ptail
.Lc4_ptail:
	s_or_b64 exec, exec, s[36:37]
	s_add_i32 s56, s56, s50
	v_add_u32_e32 v141, s56, v120
	s_add_i32 s53, s53, 1
	v_readfirstlane_b32 s36, v141
	s_mov_b32 m0, s36
	s_mov_b64 s[36:37], -1
	global_load_lds_dwordx4 v[118:119], off
	s_mul_i32 s66, s53, 9
	s_add_i32 s66, s66, -8
	s_lshr_b32 s66, s66, 1
	s_add_i32 s66, s66, 1
	s_cmp_gt_u32 s53, 7
	s_cselect_b32 s66, 0x3e8, s66
	s_mov_b32 s67, 2

	.amdhsa_kernel _Z6conv_kILi512ELi256ELi3ELi64ELi1ELi1ELb0EEvPKDF16_S1_PKfS3_PDF16_S4_S1_fS3_S3_S3_S3_
		.amdhsa_group_segment_fixed_size 163840
		.amdhsa_private_segment_fixed_size 0
		.amdhsa_kernarg_size 96
		.amdhsa_user_sgpr_count 2
		.amdhsa_user_sgpr_dispatch_ptr 0
		.amdhsa_user_sgpr_queue_ptr 0
		.amdhsa_user_sgpr_kernarg_segment_ptr 1
		.amdhsa_user_sgpr_dispatch_id 0
		.amdhsa_user_sgpr_kernarg_preload_length 0
		.amdhsa_user_sgpr_kernarg_preload_offset 0
		.amdhsa_user_sgpr_private_segment_size 0
		.amdhsa_uses_dynamic_stack 0
		.amdhsa_enable_private_segment 0
		.amdhsa_system_sgpr_workgroup_id_x 1
		.amdhsa_system_sgpr_workgroup_id_y 0
		.amdhsa_system_sgpr_workgroup_id_z 0
		.amdhsa_system_sgpr_workgroup_info 0
		.amdhsa_system_vgpr_workitem_id 0
		.amdhsa_next_free_vgpr 184
		.amdhsa_next_free_sgpr 96
		.amdhsa_accum_offset 184
		.amdhsa_reserve_vcc 1
		.amdhsa_float_round_mode_32 0
		.amdhsa_float_round_mode_16_64 0
		.amdhsa_float_denorm_mode_32 3
		.amdhsa_float_denorm_mode_16_64 3
		.amdhsa_dx10_clamp 1
		.amdhsa_ieee_mode 1
		.amdhsa_fp16_overflow 0
		.amdhsa_tg_split 0
		.amdhsa_exception_fp_ieee_invalid_op 0
		.amdhsa_exception_fp_denorm_src 0
		.amdhsa_exception_fp_ieee_div_zero 0
		.amdhsa_exception_fp_ieee_overflow 0
		.amdhsa_exception_fp_ieee_underflow 0
		.amdhsa_exception_fp_ieee_inexact 0
		.amdhsa_exception_int_div_zero 0
	.end_amdhsa_kernel

_Z6conv_kILi128ELi64ELi20ELi64ELi4ELi4ELb0EEvPKDF16_S1_PKfS3_PDF16_S4_S1_fS3_S3_S3_S3_:
	v_readfirstlane_b32 s37, v0
	v_bfe_u32 v10, v0, 3, 3
	v_and_b32_e32 v1, 7, v0
	s_and_b32 s36, s2, 3
	s_ashr_i32 s35, s2, 6
	s_lshl_b32 s3, s2, 3
	s_lshr_b32 s42, s37, 6
	s_and_b32 s33, s2, 56
	v_bitop3_b32 v2, v10, v1, 6 bitop3:0x6c
	s_mul_i32 s2, s36, 5
	v_lshlrev_b32_e32 v4, 3, v2
	s_add_i32 s24, s2, s33
	v_lshl_or_b32 v2, s42, 3, v10
	s_mov_b32 s2, 0x28282829
	s_load_dwordx2 s[28:29], s[0:1], 0x0
	s_load_dwordx2 s[4:5], s[0:1], 0x30
	v_mul_hi_u32 v3, v2, s2
	s_and_b32 s34, s3, 32
	v_lshrrev_b32_e32 v3, 3, v3
	s_movk_i32 s8, 0xffcd
	s_add_i32 s24, s24, -9
	v_mul_lo_u32 v5, v3, s8
	v_add_u32_e32 v103, s24, v3
	s_add_i32 s25, s34, -9
	s_movk_i32 s9, 0x264
	v_add3_u32 v5, s25, v2, v5
	v_cmp_gt_u32_e32 vcc, s9, v2
	v_cmp_gt_u32_e64 s[2:3], 64, v103
	s_and_b64 s[2:3], vcc, s[2:3]
	v_cmp_gt_u32_e32 vcc, 64, v5
	v_and_b32_e32 v102, 63, v0
	s_and_b64 s[6:7], s[2:3], vcc
	s_waitcnt lgkmcnt(0)
	v_mov_b64_e32 v[6:7], s[4:5]
	v_lshlrev_b32_e32 v2, 1, v4
	s_and_saveexec_b64 s[2:3], s[6:7]
	s_lshl_b32 s10, s35, 13
	v_lshlrev_b32_e32 v3, 6, v103
	v_or3_b32 v6, v3, s10, v5
	v_ashrrev_i32_e32 v7, 31, v6
	v_lshlrev_b64 v[6:7], 7, v[6:7]
	v_lshl_add_u64 v[6:7], s[28:29], 0, v[6:7]
	v_mov_b32_e32 v3, 0
	v_lshl_add_u64 v[6:7], v[6:7], 0, v[2:3]
	s_or_b64 exec, exec, s[2:3]
	s_lshl_b32 s44, s42, 10
	v_lshlrev_b32_e32 v104, 4, v102
	v_or_b32_e32 v3, s44, v104
	s_add_i32 s11, s42, 8
	v_readfirstlane_b32 s2, v3
	s_mov_b32 m0, s2
	v_lshl_or_b32 v3, s11, 3, v10
	global_load_lds_dwordx4 v[6:7], off
	s_mov_b32 s10, 0x50505051
	v_mul_hi_u32 v6, v3, s10
	v_lshrrev_b32_e32 v6, 4, v6
	v_mul_lo_u32 v7, v6, s8
	v_add_u32_e32 v105, s24, v6
	v_add3_u32 v8, s25, v3, v7
	v_cmp_gt_u32_e32 vcc, s9, v3
	v_cmp_gt_u32_e64 s[2:3], 64, v105
	s_and_b64 s[2:3], vcc, s[2:3]
	v_cmp_gt_u32_e32 vcc, 64, v8
	s_and_b64 s[8:9], s[2:3], vcc
	v_mov_b64_e32 v[6:7], s[4:5]
	s_and_saveexec_b64 s[2:3], s[8:9]
	s_lshl_b32 s12, s35, 13
	v_lshlrev_b32_e32 v3, 6, v105
	v_or3_b32 v6, v3, s12, v8
	v_ashrrev_i32_e32 v7, 31, v6
	v_lshlrev_b64 v[6:7], 7, v[6:7]
	v_lshl_add_u64 v[6:7], s[28:29], 0, v[6:7]
	v_mov_b32_e32 v3, 0
	v_lshl_add_u64 v[6:7], v[6:7], 0, v[2:3]
	s_or_b64 exec, exec, s[2:3]
	s_lshl_b32 s45, s11, 10
	v_or_b32_e32 v3, s45, v104
	s_add_i32 s14, s42, 16
	v_readfirstlane_b32 s2, v3
	s_mov_b32 m0, s2
	v_lshl_or_b32 v3, s14, 3, v10
	global_load_lds_dwordx4 v[6:7], off
	v_mul_hi_u32 v6, v3, s10
	v_lshrrev_b32_e32 v6, 4, v6
	s_movk_i32 s12, 0xffcd
	v_mul_lo_u32 v7, v6, s12
	v_add_u32_e32 v106, s24, v6
	s_movk_i32 s13, 0x264
	v_add3_u32 v9, s25, v3, v7
	v_cmp_gt_u32_e32 vcc, s13, v3
	v_cmp_gt_u32_e64 s[2:3], 64, v106
	s_and_b64 s[2:3], vcc, s[2:3]
	v_cmp_gt_u32_e32 vcc, 64, v9
	s_and_b64 s[10:11], s[2:3], vcc
	v_mov_b64_e32 v[6:7], s[4:5]
	s_and_saveexec_b64 s[2:3], s[10:11]
	s_lshl_b32 s15, s35, 13
	v_lshlrev_b32_e32 v3, 6, v106
	v_or3_b32 v6, v3, s15, v9
	v_ashrrev_i32_e32 v7, 31, v6
	v_lshlrev_b64 v[6:7], 7, v[6:7]
	v_lshl_add_u64 v[6:7], s[28:29], 0, v[6:7]
	v_mov_b32_e32 v3, 0
	v_lshl_add_u64 v[6:7], v[6:7], 0, v[2:3]
	s_or_b64 exec, exec, s[2:3]
	s_lshl_b32 s46, s14, 10
	v_or_b32_e32 v3, s46, v104
	s_add_i32 s15, s42, 24
	v_readfirstlane_b32 s2, v3
	s_mov_b32 m0, s2
	v_lshl_or_b32 v3, s15, 3, v10
	global_load_lds_dwordx4 v[6:7], off
	s_mov_b32 s14, 0x50505051
	v_mul_hi_u32 v6, v3, s14
	v_lshrrev_b32_e32 v6, 4, v6
	v_mul_lo_u32 v7, v6, s12
	v_add_u32_e32 v107, s24, v6
	v_add3_u32 v11, s25, v3, v7
	v_cmp_gt_u32_e32 vcc, s13, v3
	v_cmp_gt_u32_e64 s[2:3], 64, v107
	s_and_b64 s[2:3], vcc, s[2:3]
	v_cmp_gt_u32_e32 vcc, 64, v11
	s_and_b64 s[12:13], s[2:3], vcc
	v_mov_b64_e32 v[6:7], s[4:5]
	s_and_saveexec_b64 s[2:3], s[12:13]
	s_lshl_b32 s16, s35, 13
	v_lshlrev_b32_e32 v3, 6, v107
	v_or3_b32 v6, v3, s16, v11
	v_ashrrev_i32_e32 v7, 31, v6
	v_lshlrev_b64 v[6:7], 7, v[6:7]
	v_lshl_add_u64 v[6:7], s[28:29], 0, v[6:7]
	v_mov_b32_e32 v3, 0
	v_lshl_add_u64 v[6:7], v[6:7], 0, v[2:3]
	s_or_b64 exec, exec, s[2:3]
	s_lshl_b32 s47, s15, 10
	v_or_b32_e32 v3, s47, v104
	s_add_i32 s18, s42, 32
	v_readfirstlane_b32 s2, v3
	s_mov_b32 m0, s2
	v_lshl_or_b32 v3, s18, 3, v10
	global_load_lds_dwordx4 v[6:7], off
	v_mul_hi_u32 v6, v3, s14
	v_lshrrev_b32_e32 v6, 4, v6
	s_movk_i32 s16, 0xffcd
	v_mul_lo_u32 v7, v6, s16
	v_add_u32_e32 v108, s24, v6
	s_movk_i32 s17, 0x264
	v_add3_u32 v12, s25, v3, v7
	v_cmp_gt_u32_e32 vcc, s17, v3
	v_cmp_gt_u32_e64 s[2:3], 64, v108
	s_and_b64 s[2:3], vcc, s[2:3]
	v_cmp_gt_u32_e32 vcc, 64, v12
	s_and_b64 s[14:15], s[2:3], vcc
	v_mov_b64_e32 v[6:7], s[4:5]
	s_and_saveexec_b64 s[2:3], s[14:15]
	s_lshl_b32 s19, s35, 13
	v_lshlrev_b32_e32 v3, 6, v108
	v_or3_b32 v6, v3, s19, v12
	v_ashrrev_i32_e32 v7, 31, v6
	v_lshlrev_b64 v[6:7], 7, v[6:7]
	v_lshl_add_u64 v[6:7], s[28:29], 0, v[6:7]
	v_mov_b32_e32 v3, 0
	v_lshl_add_u64 v[6:7], v[6:7], 0, v[2:3]
	s_or_b64 exec, exec, s[2:3]
	s_lshl_b32 s48, s18, 10
	v_or_b32_e32 v3, s48, v104
	s_add_i32 s19, s42, 40
	v_readfirstlane_b32 s2, v3
	s_mov_b32 m0, s2
	v_lshl_or_b32 v3, s19, 3, v10
	global_load_lds_dwordx4 v[6:7], off
	s_mov_b32 s18, 0x50505051
	v_mul_hi_u32 v6, v3, s18
	v_lshrrev_b32_e32 v6, 4, v6
	v_mul_lo_u32 v7, v6, s16
	v_add_u32_e32 v109, s24, v6
	v_add3_u32 v13, s25, v3, v7
	v_cmp_gt_u32_e32 vcc, s17, v3
	v_cmp_gt_u32_e64 s[2:3], 64, v109
	s_and_b64 s[2:3], vcc, s[2:3]
	v_cmp_gt_u32_e32 vcc, 64, v13
	s_and_b64 s[16:17], s[2:3], vcc
	v_mov_b64_e32 v[6:7], s[4:5]
	s_and_saveexec_b64 s[2:3], s[16:17]
	s_lshl_b32 s20, s35, 13
	v_lshlrev_b32_e32 v3, 6, v109
	v_or3_b32 v6, v3, s20, v13
	v_ashrrev_i32_e32 v7, 31, v6
	v_lshlrev_b64 v[6:7], 7, v[6:7]
	v_lshl_add_u64 v[6:7], s[28:29], 0, v[6:7]
	v_mov_b32_e32 v3, 0
	v_lshl_add_u64 v[6:7], v[6:7], 0, v[2:3]
	s_or_b64 exec, exec, s[2:3]
	s_lshl_b32 s49, s19, 10
	v_or_b32_e32 v3, s49, v104
	s_add_i32 s22, s42, 48
	v_readfirstlane_b32 s2, v3
	s_mov_b32 m0, s2
	v_lshl_or_b32 v3, s22, 3, v10
	global_load_lds_dwordx4 v[6:7], off
	v_mul_hi_u32 v6, v3, s18
	v_lshrrev_b32_e32 v6, 4, v6
	s_movk_i32 s20, 0xffcd
	v_mul_lo_u32 v7, v6, s20
	v_add_u32_e32 v110, s24, v6
	s_movk_i32 s21, 0x264
	v_add3_u32 v14, s25, v3, v7
	v_cmp_gt_u32_e32 vcc, s21, v3
	v_cmp_gt_u32_e64 s[2:3], 64, v110
	s_and_b64 s[2:3], vcc, s[2:3]
	v_cmp_gt_u32_e32 vcc, 64, v14
	s_and_b64 s[18:19], s[2:3], vcc
	v_mov_b64_e32 v[6:7], s[4:5]
	s_and_saveexec_b64 s[2:3], s[18:19]
	s_lshl_b32 s23, s35, 13
	v_lshlrev_b32_e32 v3, 6, v110
	v_or3_b32 v6, v3, s23, v14
	v_ashrrev_i32_e32 v7, 31, v6
	v_lshlrev_b64 v[6:7], 7, v[6:7]
	v_lshl_add_u64 v[6:7], s[28:29], 0, v[6:7]
	v_mov_b32_e32 v3, 0
	v_lshl_add_u64 v[6:7], v[6:7], 0, v[2:3]
	s_or_b64 exec, exec, s[2:3]
	s_lshl_b32 s50, s22, 10
	v_or_b32_e32 v3, s50, v104
	s_add_i32 s23, s42, 56
	v_readfirstlane_b32 s2, v3
	s_mov_b32 m0, s2
	v_lshl_or_b32 v3, s23, 3, v10
	global_load_lds_dwordx4 v[6:7], off
	s_mov_b32 s22, 0x50505051
	v_mul_hi_u32 v6, v3, s22
	v_lshrrev_b32_e32 v6, 4, v6
	v_mul_lo_u32 v7, v6, s20
	v_add_u32_e32 v113, s24, v6
	v_add3_u32 v15, s25, v3, v7
	v_cmp_gt_u32_e32 vcc, s21, v3
	v_cmp_gt_u32_e64 s[2:3], 64, v113
	s_and_b64 s[2:3], vcc, s[2:3]
	v_cmp_gt_u32_e32 vcc, 64, v15
	s_and_b64 s[20:21], s[2:3], vcc
	v_mov_b64_e32 v[6:7], s[4:5]
	s_and_saveexec_b64 s[2:3], s[20:21]
	s_lshl_b32 s26, s35, 13
	v_lshlrev_b32_e32 v3, 6, v113
	v_or3_b32 v6, v3, s26, v15
	v_ashrrev_i32_e32 v7, 31, v6
	v_lshlrev_b64 v[6:7], 7, v[6:7]
	v_lshl_add_u64 v[6:7], s[28:29], 0, v[6:7]
	v_mov_b32_e32 v3, 0
	v_lshl_add_u64 v[6:7], v[6:7], 0, v[2:3]
	s_or_b64 exec, exec, s[2:3]
	s_lshl_b32 s51, s23, 10
	v_or_b32_e32 v3, s51, v104
	s_add_i32 s26, s42, 64
	v_readfirstlane_b32 s2, v3
	s_mov_b32 m0, s2
	v_lshl_or_b32 v3, s26, 3, v10
	global_load_lds_dwordx4 v[6:7], off
	v_mul_hi_u32 v6, v3, s22
	v_lshrrev_b32_e32 v6, 4, v6
	s_movk_i32 s2, 0xffcd
	v_mul_lo_u32 v7, v6, s2
	v_add_u32_e32 v114, s24, v6
	s_movk_i32 s2, 0x264
	v_add3_u32 v16, s25, v3, v7
	v_cmp_gt_u32_e32 vcc, s2, v3
	v_cmp_gt_u32_e64 s[2:3], 64, v114
	s_and_b64 s[2:3], vcc, s[2:3]
	v_cmp_gt_u32_e32 vcc, 64, v16
	s_and_b64 s[22:23], s[2:3], vcc
	s_xor_b64 s[2:3], s[22:23], -1
	s_and_saveexec_b64 s[30:31], s[2:3]
	s_xor_b64 s[2:3], exec, s[30:31]
	s_lshl_b32 s27, s35, 13
	s_or_saveexec_b64 s[2:3], s[2:3]
	v_mov_b32_e32 v17, s27
	v_mov_b64_e32 v[6:7], s[4:5]
	s_xor_b64 exec, exec, s[2:3]
	s_lshl_b32 s27, s35, 13
	v_lshlrev_b32_e32 v3, 6, v114
	v_or3_b32 v6, v3, s27, v16
	v_ashrrev_i32_e32 v7, 31, v6
	v_lshlrev_b64 v[6:7], 7, v[6:7]
	v_lshl_add_u64 v[6:7], s[28:29], 0, v[6:7]
	v_mov_b32_e32 v3, 0
	v_lshl_add_u64 v[6:7], v[6:7], 0, v[2:3]
	v_mov_b32_e32 v17, s27
	s_or_b64 exec, exec, s[2:3]
	s_lshl_b32 s38, s26, 10
	v_or_b32_e32 v2, s38, v104
	s_add_i32 s41, s42, 0x48
	v_readfirstlane_b32 s2, v2
	s_mov_b32 m0, s2
	v_lshl_or_b32 v2, s41, 3, v10
	global_load_lds_dwordx4 v[6:7], off
	s_mov_b32 s2, 0x50505051
	v_mul_hi_u32 v3, v2, s2
	v_lshrrev_b32_e32 v3, 4, v3
	s_movk_i32 s2, 0xffcd
	s_load_dwordx2 s[30:31], s[0:1], 0x8
	v_mul_lo_u32 v6, v3, s2
	v_add_u32_e32 v115, s24, v3
	s_movk_i32 s2, 0x264
	v_add3_u32 v6, s25, v2, v6
	v_cmp_gt_u32_e32 vcc, s2, v2
	v_cmp_gt_u32_e64 s[2:3], 64, v115
	s_and_b64 s[2:3], vcc, s[2:3]
	v_cmp_gt_u32_e32 vcc, 64, v6
	s_and_b64 s[24:25], s[2:3], vcc
	s_xor_b64 s[2:3], s[24:25], -1
	s_and_saveexec_b64 s[26:27], s[2:3]
	s_xor_b64 s[2:3], exec, s[26:27]
	s_or_saveexec_b64 s[26:27], s[2:3]
	s_load_dwordx2 s[2:3], s[0:1], 0x28
	v_mov_b64_e32 v[2:3], s[4:5]
	s_xor_b64 exec, exec, s[26:27]
	v_lshlrev_b32_e32 v2, 6, v115
	v_or3_b32 v2, v2, v17, v6
	v_ashrrev_i32_e32 v3, 31, v2
	v_lshlrev_b64 v[2:3], 7, v[2:3]
	v_lshl_add_u64 v[2:3], s[28:29], 0, v[2:3]
	v_lshlrev_b32_e32 v18, 1, v4
	v_mov_b32_e32 v19, 0
	v_lshl_add_u64 v[2:3], v[2:3], 0, v[18:19]
	s_or_b64 exec, exec, s[26:27]
	v_lshrrev_b32_e32 v112, 4, v102
	v_lshl_or_b32 v7, v10, 6, s44
	v_bitop3_b32 v10, v112, v0, 6 bitop3:0x78
	v_and_b32_e32 v111, 15, v0
	v_lshlrev_b32_e32 v10, 4, v10
	s_lshr_b32 s40, s37, 8
	v_lshl_or_b32 v10, v111, 7, v10
	v_lshl_or_b32 v10, s40, 13, v10
	s_lshl_b32 s41, s41, 10
	s_movk_i32 s26, 0xdc0
	v_add_u32_e32 v118, 0x14000, v10
	v_or_b32_e32 v10, s41, v104
	v_and_or_b32 v7, v7, s26, v4
	v_readfirstlane_b32 s26, v10
	s_mov_b32 m0, s26
	s_lshl_b32 s55, s42, 11
	s_mul_hi_u32 s26, s37, 0x51eb851f
	s_and_b32 s39, s42, 3
	s_add_i32 s42, s55, 0x14000
	s_lshr_b32 s27, s26, 13
	s_lshr_b32 s52, s26, 14
	s_bitcmp1_b32 s26, 13
	s_cselect_b32 s26, 0x190, 0
	s_sub_i32 s27, s36, s27
	s_add_i32 s27, s27, s52
	s_mulk_i32 s27, 0x64
	s_add_i32 s26, s26, s40
	s_add_i32 s26, s26, s27
	s_ashr_i32 s27, s26, 31
	s_lshl_b64 s[26:27], s[26:27], 13
	s_waitcnt lgkmcnt(0)
	s_add_u32 s26, s30, s26
	s_addc_u32 s27, s31, s27
	s_add_i32 s52, s40, 2
	global_load_lds_dwordx4 v[2:3], off
	v_lshlrev_b32_e32 v2, 1, v7
	s_mov_b32 m0, s42
	s_mul_hi_u32 s53, s52, 0x28f5c29
	global_load_lds_dwordx4 v2, s[26:27]
	s_add_i32 m0, s55, 0x14400
	s_lshr_b32 s56, s53, 1
	s_bitcmp1_b32 s53, 0
	s_cselect_b32 s57, 0x190, 0
	s_sub_i32 s53, s36, s53
	s_add_i32 s53, s53, s56
	s_mulk_i32 s53, 0x64
	s_add_i32 s52, s57, s52
	s_add_i32 s52, s52, s53
	v_mov_b32_e32 v3, 0
	s_ashr_i32 s53, s52, 31
	v_lshl_add_u64 v[18:19], s[26:27], 0, v[2:3]
	s_mov_b64 s[26:27], 0x400
	s_lshl_b64 s[52:53], s[52:53], 13
	v_lshl_add_u64 v[18:19], v[18:19], 0, s[26:27]
	s_add_u32 s52, s30, s52
	global_load_lds_dwordx4 v[18:19], off
	s_addc_u32 s53, s31, s53
	s_add_i32 m0, s55, 0x18000
	v_lshl_add_u64 v[18:19], s[52:53], 0, v[2:3]
	global_load_lds_dwordx4 v2, s[52:53]
	s_add_i32 s52, s40, 4
	s_mul_hi_u32 s53, s52, 0x28f5c29
	s_add_i32 m0, s55, 0x18400
	s_lshr_b32 s56, s53, 1
	s_bitcmp1_b32 s53, 0
	s_cselect_b32 s57, 0x190, 0
	s_sub_i32 s53, s36, s53
	s_add_i32 s53, s53, s56
	s_mulk_i32 s53, 0x64
	s_add_i32 s52, s57, s52
	s_add_i32 s52, s52, s53
	s_ashr_i32 s53, s52, 31
	s_lshl_b64 s[52:53], s[52:53], 13
	s_add_u32 s52, s30, s52
	v_lshl_add_u64 v[18:19], v[18:19], 0, s[26:27]
	s_addc_u32 s53, s31, s53
	global_load_lds_dwordx4 v[18:19], off
	s_add_i32 m0, s55, 0x1c000
	v_lshl_add_u64 v[18:19], s[52:53], 0, v[2:3]
	global_load_lds_dwordx4 v2, s[52:53]
	v_lshl_add_u64 v[18:19], v[18:19], 0, s[26:27]
	s_add_i32 m0, s55, 0x1c400
	s_mul_hi_u32 s52, s40, 0x28f5c29
	global_load_lds_dwordx4 v[18:19], off
	s_mulk_i32 s52, 0x64
	s_sub_i32 s52, s40, s52
	s_mul_i32 s53, s52, 0x67
	s_bfe_u32 s53, s53, 0x5000b
	s_mul_i32 s53, s53, 31
	s_mul_i32 s54, s39, 0x66
	s_and_b32 s53, s53, 0xff
	v_add_u32_e32 v116, s54, v111
	s_add_i32 s52, s52, s53
	s_waitcnt vmcnt(4) lgkmcnt(0)
	s_barrier
	ds_read_b128 v[66:69], v118
	v_add_u32_e32 v7, s52, v116
	v_add_u32_e32 v117, 51, v116
	ds_read_b128 v[70:73], v118 offset:2048
	v_lshlrev_b32_e32 v10, 7, v7
	v_bitop3_b32 v7, v7, v112, 6 bitop3:0x6c
	v_lshl_or_b32 v139, v7, 4, v10
	ds_read_b128 v[74:77], v139
	v_add_u32_e32 v7, s52, v117
	ds_read_b128 v[78:81], v139 offset:2048
	v_lshlrev_b32_e32 v10, 7, v7
	v_bitop3_b32 v7, v7, v112, 6 bitop3:0x6c
	v_lshl_or_b32 v140, v7, 4, v10
	ds_read_b128 v[86:89], v140
	ds_read_b128 v[82:85], v140 offset:2048
	ds_read_b128 v[94:97], v118 offset:4096
	ds_read_b128 v[90:93], v118 offset:6144
	v_add_u32_e32 v120, v17, v5
	v_lshlrev_b32_e32 v4, 1, v4
	v_mov_b32_e32 v5, v3
	v_lshl_add_u64 v[98:99], s[28:29], 0, v[4:5]
	s_add_i32 s28, s40, s54
	v_xor_b32_e32 v119, 64, v118
	s_mov_b32 s43, 0
	v_add_u32_e32 v121, v17, v8
	v_add_u32_e32 v122, v17, v9
	v_add_u32_e32 v123, v17, v11
	v_add_u32_e32 v124, v17, v12
	v_add_u32_e32 v125, v17, v13
	v_add_u32_e32 v126, v17, v14
	v_add_u32_e32 v127, v17, v15
	v_add_u32_e32 v128, v17, v16
	v_add_u32_e32 v129, v17, v6
	v_lshl_add_u64 v[100:101], s[30:31], 0, v[2:3]
	v_add_u32_e32 v130, s28, v111
	v_add_u32_e32 v131, s44, v104
	v_add_u32_e32 v132, s45, v104
	v_add_u32_e32 v133, s46, v104
	v_add_u32_e32 v134, s47, v104
	v_add_u32_e32 v135, s48, v104
	v_add_u32_e32 v136, s49, v104
	v_add_u32_e32 v137, s50, v104
	v_add_u32_e32 v138, s51, v104
	s_mov_b32 s30, s40
	s_mov_b32 s31, s40
	s_mov_b32 s44, 0
	s_mov_b32 s45, 0
	v_mov_b32_e32 v2, v3
	v_mov_b32_e32 v4, v3
	v_mov_b32_e32 v6, v3
	v_mov_b32_e32 v7, v3
	v_mov_b32_e32 v8, v3
	v_mov_b32_e32 v9, v3
	v_mov_b32_e32 v14, v3
	v_mov_b32_e32 v15, v3
	v_mov_b32_e32 v16, v3
	v_mov_b32_e32 v17, v3
	v_mov_b32_e32 v30, v3
	v_mov_b32_e32 v31, v3
	v_mov_b32_e32 v32, v3
	v_mov_b32_e32 v33, v3
	v_mov_b32_e32 v34, v3
	v_mov_b32_e32 v35, v3
	v_mov_b32_e32 v36, v3
	v_mov_b32_e32 v37, v3
	v_mov_b32_e32 v38, v3
	v_mov_b32_e32 v39, v3
	v_mov_b32_e32 v40, v3
	v_mov_b32_e32 v41, v3
	v_mov_b32_e32 v42, v3
	v_mov_b32_e32 v43, v3
	v_mov_b32_e32 v44, v3
	v_mov_b32_e32 v45, v3
	v_mov_b32_e32 v46, v3
	v_mov_b32_e32 v47, v3
	v_mov_b32_e32 v48, v3
	v_mov_b32_e32 v49, v3
	v_mov_b32_e32 v50, v3
	v_mov_b32_e32 v51, v3
	v_mov_b32_e32 v52, v3
	v_mov_b32_e32 v53, v3
	v_mov_b32_e32 v54, v3
	v_mov_b32_e32 v55, v3
	v_mov_b32_e32 v56, v3
	v_mov_b32_e32 v57, v3
	v_mov_b32_e32 v58, v3
	v_mov_b32_e32 v59, v3
	v_mov_b32_e32 v60, v3
	v_mov_b32_e32 v61, v3
	v_mov_b32_e32 v62, v3
	v_mov_b32_e32 v63, v3
	v_mov_b32_e32 v64, v3
	v_mov_b32_e32 v65, v3
	v_mov_b32_e32 v26, v3
	v_mov_b32_e32 v27, v3
	v_mov_b32_e32 v28, v3
	v_mov_b32_e32 v29, v3
	v_mov_b32_e32 v18, v3
	v_mov_b32_e32 v19, v3
	v_mov_b32_e32 v20, v3
	v_mov_b32_e32 v21, v3
	v_mov_b32_e32 v22, v3
	v_mov_b32_e32 v23, v3
	v_mov_b32_e32 v24, v3
	v_mov_b32_e32 v25, v3
	v_mov_b32_e32 v10, v3
	v_mov_b32_e32 v11, v3
	v_mov_b32_e32 v12, v3
	v_mov_b32_e32 v13, v3
	s_mov_b32 s60, 0
	s_mov_b32 s61, 50
	s_add_i32 s62, s40, 2
	s_mov_b32 s63, 1
	s_mov_b32 s65, 0
	s_mul_i32 s73, s36, 0x64
	s_add_i32 s73, s73, s40
	s_add_i32 s67, s73, 6
	s_lshl_b32 s64, s67, 13
	v_lshl_add_u64 v[174:175], v[100:101], 0, s[64:65]
	s_add_i32 s69, s42, 0xc000
	v_lshl_add_u64 v[176:177], v[174:175], 0, s[26:27]
	v_mov_b32_e32 v183, v119
.Lc6_loop:
	s_waitcnt vmcnt(2)
	s_barrier
	s_waitcnt lgkmcnt(5)
	v_mfma_f32_16x16x32_f16 v[62:65], v[66:69], v[74:77], v[62:65]
	ds_read_b128 v[142:145], v183
	v_mfma_f32_16x16x32_f16 v[58:61], v[70:73], v[74:77], v[58:61]
	v_xor_b32_e32 v180, 64, v139
	s_waitcnt lgkmcnt(5)
	v_mfma_f32_16x16x32_f16 v[46:49], v[66:69], v[78:81], v[46:49]
	ds_read_b128 v[146:149], v183 offset:2048
	v_mfma_f32_16x16x32_f16 v[42:45], v[70:73], v[78:81], v[42:45]
	v_xor_b32_e32 v181, 64, v140
	s_mov_b32 m0, s69
	s_add_i32 s70, s43, 0x4000
	global_load_lds_dwordx4 v[174:175], off
	s_waitcnt lgkmcnt(5)
	v_mfma_f32_16x16x32_f16 v[30:33], v[66:69], v[86:89], v[30:33]
	ds_read_b128 v[150:153], v180
	v_mfma_f32_16x16x32_f16 v[14:17], v[70:73], v[86:89], v[14:17]
	s_and_b32 s70, s70, 0xc000
	s_add_i32 s71, s69, 0x400
	s_waitcnt lgkmcnt(5)
	v_mfma_f32_16x16x32_f16 v[26:29], v[66:69], v[82:85], v[26:29]
	ds_read_b128 v[154:157], v180 offset:2048
	v_mfma_f32_16x16x32_f16 v[18:21], v[70:73], v[82:85], v[18:21]
	v_add_u32_e32 v182, s70, v118
	s_waitcnt lgkmcnt(5)
	v_mfma_f32_16x16x32_f16 v[54:57], v[94:97], v[74:77], v[54:57]
	ds_read_b128 v[158:161], v181
	s_waitcnt lgkmcnt(5)
	v_mfma_f32_16x16x32_f16 v[50:53], v[90:93], v[74:77], v[50:53]
	v_mfma_f32_16x16x32_f16 v[38:41], v[94:97], v[78:81], v[38:41]
	ds_read_b128 v[162:165], v181 offset:2048
	v_mfma_f32_16x16x32_f16 v[34:37], v[90:93], v[78:81], v[34:37]
	v_add_u32_e32 v178, s62, v116
	v_mfma_f32_16x16x32_f16 v[6:9], v[94:97], v[86:89], v[6:9]
	ds_read_b128 v[166:169], v183 offset:4096
	v_mfma_f32_16x16x32_f16 v[2:5], v[90:93], v[86:89], v[2:5]
	v_lshlrev_b32_e32 v179, 7, v178
	v_bitop3_b32 v178, v178, v112, 6 bitop3:0x6c
	v_mfma_f32_16x16x32_f16 v[22:25], v[94:97], v[82:85], v[22:25]
	ds_read_b128 v[170:173], v183 offset:6144
	v_mfma_f32_16x16x32_f16 v[10:13], v[90:93], v[82:85], v[10:13]
	v_lshl_or_b32 v139, v178, 4, v179
	v_add_u32_e32 v183, s70, v119
	s_waitcnt lgkmcnt(5)
	v_mfma_f32_16x16x32_f16 v[62:65], v[142:145], v[150:153], v[62:65]
	ds_read_b128 v[66:69], v182
	v_mfma_f32_16x16x32_f16 v[58:61], v[146:149], v[150:153], v[58:61]
	s_mov_b32 m0, s71
	s_add_i32 s63, s63, 1
	global_load_lds_dwordx4 v[176:177], off
	s_waitcnt lgkmcnt(5)
	v_mfma_f32_16x16x32_f16 v[46:49], v[142:145], v[154:157], v[46:49]
	ds_read_b128 v[70:73], v182 offset:2048
	v_mfma_f32_16x16x32_f16 v[42:45], v[146:149], v[154:157], v[42:45]
	v_add_u32_e32 v178, s62, v117
	s_waitcnt lgkmcnt(5)
	v_mfma_f32_16x16x32_f16 v[30:33], v[142:145], v[158:161], v[30:33]
	ds_read_b128 v[74:77], v139
	v_mfma_f32_16x16x32_f16 v[14:17], v[146:149], v[158:161], v[14:17]
	v_lshlrev_b32_e32 v179, 7, v178
	v_bitop3_b32 v178, v178, v112, 6 bitop3:0x6c
	s_waitcnt lgkmcnt(5)
	v_mfma_f32_16x16x32_f16 v[26:29], v[142:145], v[162:165], v[26:29]
	ds_read_b128 v[78:81], v139 offset:2048
	v_mfma_f32_16x16x32_f16 v[18:21], v[146:149], v[162:165], v[18:21]
	v_lshl_or_b32 v140, v178, 4, v179
	s_waitcnt lgkmcnt(5)
	v_mfma_f32_16x16x32_f16 v[54:57], v[166:169], v[150:153], v[54:57]
	ds_read_b128 v[86:89], v140
	s_waitcnt lgkmcnt(5)
	v_mfma_f32_16x16x32_f16 v[50:53], v[170:173], v[150:153], v[50:53]
	s_cmp_lg_u32 s63, 10
	s_cselect_b32 s72, 2, 33
	s_cselect_b32 s63, s63, 0
	s_add_i32 s62, s62, s72
	v_mfma_f32_16x16x32_f16 v[38:41], v[166:169], v[154:157], v[38:41]
	ds_read_b128 v[82:85], v140 offset:2048
	v_mfma_f32_16x16x32_f16 v[34:37], v[170:173], v[154:157], v[34:37]
	s_addk_i32 s43, 0x4000
	s_add_i32 s60, s60, 1
	s_add_i32 s66, s60, 3
	s_cmpk_lt_u32 s60, 0x61
	s_cselect_b32 s66, s66, 0x63
	s_lshl_b32 s67, s66, 1
	s_cmpk_gt_u32 s66, 49
	s_cselect_b32 s68, 0x12c, 0
	s_add_i32 s67, s67, s68
	v_mfma_f32_16x16x32_f16 v[6:9], v[166:169], v[158:161], v[6:9]
	ds_read_b128 v[94:97], v182 offset:4096
	s_add_i32 s67, s67, s73
	s_lshl_b32 s64, s67, 13
	v_mfma_f32_16x16x32_f16 v[2:5], v[170:173], v[158:161], v[2:5]
	v_lshl_add_u64 v[174:175], v[100:101], 0, s[64:65]
	s_add_i32 s69, s43, 0xc000
	s_and_b32 s69, s69, 0xc000
	s_add_i32 s69, s69, s42
	v_mfma_f32_16x16x32_f16 v[22:25], v[166:169], v[162:165], v[22:25]
	ds_read_b128 v[90:93], v182 offset:6144
	v_lshl_add_u64 v[176:177], v[174:175], 0, s[26:27]
	s_cmp_eq_u32 s60, s61
	v_mfma_f32_16x16x32_f16 v[10:13], v[170:173], v[162:165], v[10:13]
	s_cbranch_scc0 .Lc6_loop
	s_cmpk_eq_i32 s61, 0x64
	s_cbranch_scc1 .LBB10_49
	s_waitcnt lgkmcnt(0)
	s_mov_b32 s46, 64
	v_mov_b64_e32 v[66:67], s[4:5]
	s_barrier
	s_and_saveexec_b64 s[28:29], s[6:7]
	v_or_b32_e32 v66, s46, v103
	v_lshl_or_b32 v66, v66, 6, v120
	v_ashrrev_i32_e32 v67, 31, v66
	v_lshlrev_b64 v[66:67], 7, v[66:67]
	v_lshl_add_u64 v[66:67], v[98:99], 0, v[66:67]
	s_or_b64 exec, exec, s[28:29]
	v_readfirstlane_b32 s28, v131
	s_mov_b32 m0, s28
	s_nop 0
	global_load_lds_dwordx4 v[66:67], off
	v_mov_b64_e32 v[66:67], s[4:5]
	s_and_saveexec_b64 s[28:29], s[8:9]
	v_or_b32_e32 v66, s46, v105
	v_lshl_or_b32 v66, v66, 6, v121
	v_ashrrev_i32_e32 v67, 31, v66
	v_lshlrev_b64 v[66:67], 7, v[66:67]
	v_lshl_add_u64 v[66:67], v[98:99], 0, v[66:67]
	s_or_b64 exec, exec, s[28:29]
	v_readfirstlane_b32 s28, v132
	s_mov_b32 m0, s28
	s_nop 0
	global_load_lds_dwordx4 v[66:67], off
	v_mov_b64_e32 v[66:67], s[4:5]
	s_and_saveexec_b64 s[28:29], s[10:11]
	v_or_b32_e32 v66, s46, v106
	v_lshl_or_b32 v66, v66, 6, v122
	v_ashrrev_i32_e32 v67, 31, v66
	v_lshlrev_b64 v[66:67], 7, v[66:67]
	v_lshl_add_u64 v[66:67], v[98:99], 0, v[66:67]
	s_or_b64 exec, exec, s[28:29]
	v_readfirstlane_b32 s28, v133
	s_mov_b32 m0, s28
	s_nop 0
	global_load_lds_dwordx4 v[66:67], off
	v_mov_b64_e32 v[66:67], s[4:5]
	s_and_saveexec_b64 s[28:29], s[12:13]
	v_or_b32_e32 v66, s46, v107
	v_lshl_or_b32 v66, v66, 6, v123
	v_ashrrev_i32_e32 v67, 31, v66
	v_lshlrev_b64 v[66:67], 7, v[66:67]
	v_lshl_add_u64 v[66:67], v[98:99], 0, v[66:67]
	s_or_b64 exec, exec, s[28:29]
	v_readfirstlane_b32 s28, v134
	s_mov_b32 m0, s28
	s_nop 0
	global_load_lds_dwordx4 v[66:67], off
	v_mov_b64_e32 v[66:67], s[4:5]
	s_and_saveexec_b64 s[28:29], s[14:15]
	v_or_b32_e32 v66, s46, v108
	v_lshl_or_b32 v66, v66, 6, v124
	v_ashrrev_i32_e32 v67, 31, v66
	v_lshlrev_b64 v[66:67], 7, v[66:67]
	v_lshl_add_u64 v[66:67], v[98:99], 0, v[66:67]
	s_or_b64 exec, exec, s[28:29]
	v_readfirstlane_b32 s28, v135
	s_mov_b32 m0, s28
	s_nop 0
	global_load_lds_dwordx4 v[66:67], off
	v_mov_b64_e32 v[66:67], s[4:5]
	s_and_saveexec_b64 s[28:29], s[16:17]
	v_or_b32_e32 v66, s46, v109
	v_lshl_or_b32 v66, v66, 6, v125
	v_ashrrev_i32_e32 v67, 31, v66
	v_lshlrev_b64 v[66:67], 7, v[66:67]
	v_lshl_add_u64 v[66:67], v[98:99], 0, v[66:67]
	s_or_b64 exec, exec, s[28:29]
	v_readfirstlane_b32 s28, v136
	s_mov_b32 m0, s28
	s_nop 0
	global_load_lds_dwordx4 v[66:67], off
	v_mov_b64_e32 v[66:67], s[4:5]
	s_and_saveexec_b64 s[28:29], s[18:19]
	v_or_b32_e32 v66, s46, v110
	v_lshl_or_b32 v66, v66, 6, v126
	v_ashrrev_i32_e32 v67, 31, v66
	v_lshlrev_b64 v[66:67], 7, v[66:67]
	v_lshl_add_u64 v[66:67], v[98:99], 0, v[66:67]
	s_or_b64 exec, exec, s[28:29]
	v_readfirstlane_b32 s28, v137
	s_mov_b32 m0, s28
	s_nop 0
	global_load_lds_dwordx4 v[66:67], off
	v_mov_b64_e32 v[66:67], s[4:5]
	s_and_saveexec_b64 s[28:29], s[20:21]
	v_or_b32_e32 v66, s46, v113
	v_lshl_or_b32 v66, v66, 6, v127
	v_ashrrev_i32_e32 v67, 31, v66
	v_lshlrev_b64 v[66:67], 7, v[66:67]
	v_lshl_add_u64 v[66:67], v[98:99], 0, v[66:67]
	s_or_b64 exec, exec, s[28:29]
	v_readfirstlane_b32 s28, v138
	s_mov_b32 m0, s28
	s_nop 0
	global_load_lds_dwordx4 v[66:67], off
	v_mov_b64_e32 v[66:67], s[4:5]
	s_and_saveexec_b64 s[28:29], s[22:23]
	v_or_b32_e32 v66, s46, v114
	v_lshl_or_b32 v66, v66, 6, v128
	v_ashrrev_i32_e32 v67, 31, v66
	v_lshlrev_b64 v[66:67], 7, v[66:67]
	v_lshl_add_u64 v[66:67], v[98:99], 0, v[66:67]
	s_or_b64 exec, exec, s[28:29]
	v_add_u32_e32 v68, s38, v104
	s_nop 0
	v_readfirstlane_b32 s28, v68
	s_mov_b32 m0, s28
	s_nop 0
	global_load_lds_dwordx4 v[66:67], off
	v_mov_b64_e32 v[66:67], s[4:5]
	s_and_saveexec_b64 s[28:29], s[24:25]
	s_cbranch_execz .Lc6_seam_tail
	v_or_b32_e32 v66, s46, v115
	v_lshl_or_b32 v66, v66, 6, v129
	v_ashrrev_i32_e32 v67, 31, v66
	v_lshlrev_b64 v[66:67], 7, v[66:67]
	v_lshl_add_u64 v[66:67], v[98:99], 0, v[66:67]
	s_branch .Lc6_seam_tail
.Lc6_seam_tail:
	s_or_b64 exec, exec, s[28:29]
	v_add_u32_e32 v68, s41, v104
	s_nop 0
	v_readfirstlane_b32 s28, v68
	s_mov_b32 m0, s28
	s_and_b32 s28, s43, 0xc000
	global_load_lds_dwordx4 v[66:67], off
	v_add_u32_e32 v178, s40, v116
	v_lshlrev_b32_e32 v179, 7, v178
	v_bitop3_b32 v180, v178, v112, 6 bitop3:0x6c
	v_lshl_or_b32 v139, v180, 4, v179
	v_add_u32_e32 v178, 51, v178
	v_lshlrev_b32_e32 v179, 7, v178
	v_bitop3_b32 v180, v178, v112, 6 bitop3:0x6c
	v_lshl_or_b32 v140, v180, 4, v179
	v_add_u32_e32 v182, s28, v118
	v_add_u32_e32 v183, s28, v119
	s_waitcnt vmcnt(0)
	s_barrier
	ds_read_b128 v[66:69], v182
	ds_read_b128 v[70:73], v182 offset:2048
	ds_read_b128 v[74:77], v139
	ds_read_b128 v[78:81], v139 offset:2048
	ds_read_b128 v[86:89], v140
	ds_read_b128 v[82:85], v140 offset:2048
	ds_read_b128 v[94:97], v182 offset:4096
	ds_read_b128 v[90:93], v182 offset:6144
	s_add_i32 s62, s40, 2
	s_mov_b32 s63, 1
	s_movk_i32 s61, 0x64
	s_branch .Lc6_loop

	.amdhsa_kernel _Z6conv_kILi128ELi64ELi20ELi64ELi4ELi4ELb0EEvPKDF16_S1_PKfS3_PDF16_S4_S1_fS3_S3_S3_S3_
		.amdhsa_group_segment_fixed_size 147456
		.amdhsa_private_segment_fixed_size 0
		.amdhsa_kernarg_size 96
		.amdhsa_user_sgpr_count 2
		.amdhsa_user_sgpr_dispatch_ptr 0
		.amdhsa_user_sgpr_queue_ptr 0
		.amdhsa_user_sgpr_kernarg_segment_ptr 1
		.amdhsa_user_sgpr_dispatch_id 0
		.amdhsa_user_sgpr_kernarg_preload_length 0
		.amdhsa_user_sgpr_kernarg_preload_offset 0
		.amdhsa_user_sgpr_private_segment_size 0
		.amdhsa_uses_dynamic_stack 0
		.amdhsa_enable_private_segment 0
		.amdhsa_system_sgpr_workgroup_id_x 1
		.amdhsa_system_sgpr_workgroup_id_y 0
		.amdhsa_system_sgpr_workgroup_id_z 0
		.amdhsa_system_sgpr_workgroup_info 0
		.amdhsa_system_vgpr_workitem_id 0
		.amdhsa_next_free_vgpr 184
		.amdhsa_next_free_sgpr 96
		.amdhsa_accum_offset 184
		.amdhsa_reserve_vcc 1
		.amdhsa_float_round_mode_32 0
		.amdhsa_float_round_mode_16_64 0
		.amdhsa_float_denorm_mode_32 3
		.amdhsa_float_denorm_mode_16_64 3
		.amdhsa_dx10_clamp 1
		.amdhsa_ieee_mode 1
		.amdhsa_fp16_overflow 0
		.amdhsa_tg_split 0
		.amdhsa_exception_fp_ieee_invalid_op 0
		.amdhsa_exception_fp_denorm_src 0
		.amdhsa_exception_fp_ieee_div_zero 0
		.amdhsa_exception_fp_ieee_overflow 0
		.amdhsa_exception_fp_ieee_underflow 0
		.amdhsa_exception_fp_ieee_inexact 0
		.amdhsa_exception_int_div_zero 0
	.end_amdhsa_kernel

amdhsa.kernels:
  - .agpr_count:     0
    .args:
      - .actual_access:  read_only
        .address_space:  global
        .offset:         0
        .size:           8
        .value_kind:     global_buffer
      - .actual_access:  read_only
        .address_space:  global
        .offset:         8
        .size:           8
        .value_kind:     global_buffer
      - .actual_access:  read_only
        .address_space:  global
        .offset:         16
        .size:           8
        .value_kind:     global_buffer
      - .actual_access:  read_only
        .address_space:  global
        .offset:         24
        .size:           8
        .value_kind:     global_buffer
      - .actual_access:  read_only
        .address_space:  global
        .offset:         32
        .size:           8
        .value_kind:     global_buffer
      - .actual_access:  read_only
        .address_space:  global
        .offset:         40
        .size:           8
        .value_kind:     global_buffer
      - .actual_access:  write_only
        .address_space:  global
        .offset:         48
        .size:           8
        .value_kind:     global_buffer
      - .actual_access:  write_only
        .address_space:  global
        .offset:         56
        .size:           8
        .value_kind:     global_buffer
      - .actual_access:  write_only
        .address_space:  global
        .offset:         64
        .size:           8
        .value_kind:     global_buffer
      - .actual_access:  write_only
        .address_space:  global
        .offset:         72
        .size:           8
        .value_kind:     global_buffer
      - .actual_access:  write_only
        .address_space:  global
        .offset:         80
        .size:           8
        .value_kind:     global_buffer
      - .actual_access:  write_only
        .address_space:  global
        .offset:         88
        .size:           8
        .value_kind:     global_buffer
      - .actual_access:  read_only
        .address_space:  global
        .offset:         96
        .size:           8
        .value_kind:     global_buffer
      - .actual_access:  read_only
        .address_space:  global
        .offset:         104
        .size:           8
        .value_kind:     global_buffer
      - .actual_access:  read_only
        .address_space:  global
        .offset:         112
        .size:           8
        .value_kind:     global_buffer
      - .actual_access:  read_only
        .address_space:  global
        .offset:         120
        .size:           8
        .value_kind:     global_buffer
      - .actual_access:  write_only
        .address_space:  global
        .offset:         128
        .size:           8
        .value_kind:     global_buffer
      - .actual_access:  write_only
        .address_space:  global
        .offset:         136
        .size:           8
        .value_kind:     global_buffer
    .group_segment_fixed_size: 14400
    .kernarg_segment_align: 8
    .kernarg_segment_size: 144
    .language:       OpenCL C
    .language_version:
      - 2
      - 0
    .max_flat_workgroup_size: 256
    .name:           _Z10prep_all_kPKfS0_S0_S0_S0_S0_PDF16_S1_S1_S1_S1_S1_S0_S0_S0_S0_S1_Pj
    .private_segment_fixed_size: 0
    .sgpr_count:     27
    .sgpr_spill_count: 0
    .symbol:         _Z10prep_all_kPKfS0_S0_S0_S0_S0_PDF16_S1_S1_S1_S1_S1_S0_S0_S0_S0_S1_Pj.kd
    .uniform_work_group_size: 1
    .uses_dynamic_stack: false
    .vgpr_count:     64
    .vgpr_spill_count: 0
    .wavefront_size: 64
  - .agpr_count:     0
    .args:
      - .actual_access:  read_only
        .address_space:  global
        .offset:         0
        .size:           8
        .value_kind:     global_buffer
      - .actual_access:  read_only
        .address_space:  global
        .offset:         8
        .size:           8
        .value_kind:     global_buffer
      - .actual_access:  read_only
        .address_space:  global
        .offset:         16
        .size:           8
        .value_kind:     global_buffer
      - .actual_access:  read_only
        .address_space:  global
        .offset:         24
        .size:           8
        .value_kind:     global_buffer
      - .actual_access:  read_only
        .address_space:  global
        .offset:         32
        .size:           8
        .value_kind:     global_buffer
      - .actual_access:  read_only
        .address_space:  global
        .offset:         40
        .size:           8
        .value_kind:     global_buffer
      - .actual_access:  write_only
        .address_space:  global
        .offset:         48
        .size:           8
        .value_kind:     global_buffer
    .group_segment_fixed_size: 0
    .kernarg_segment_align: 8
    .kernarg_segment_size: 56
    .language:       OpenCL C
    .language_version:
      - 2
      - 0
    .max_flat_workgroup_size: 256
    .name:           _Z9finish6_kPKDF16_PKfS2_S2_S2_S2_Pf
    .private_segment_fixed_size: 0
    .sgpr_count:     18
    .sgpr_spill_count: 0
    .symbol:         _Z9finish6_kPKDF16_PKfS2_S2_S2_S2_Pf.kd
    .uniform_work_group_size: 1
    .uses_dynamic_stack: false
    .vgpr_count:     51
    .vgpr_spill_count: 0
    .wavefront_size: 64
  - .agpr_count:     0
    .args:
      - .actual_access:  read_only
        .address_space:  global
        .offset:         0
        .size:           8
        .value_kind:     global_buffer
      - .actual_access:  write_only
        .address_space:  global
        .offset:         8
        .size:           8
        .value_kind:     global_buffer
    .group_segment_fixed_size: 16640
    .kernarg_segment_align: 8
    .kernarg_segment_size: 16
    .language:       OpenCL C
    .language_version:
      - 2
      - 0
    .max_flat_workgroup_size: 256
    .name:           _Z6gram_kPKfPf
    .private_segment_fixed_size: 0
    .sgpr_count:     16
    .sgpr_spill_count: 0
    .symbol:         _Z6gram_kPKfPf.kd
    .uniform_work_group_size: 1
    .uses_dynamic_stack: false
    .vgpr_count:     38
    .vgpr_spill_count: 0
    .wavefront_size: 64
  - .agpr_count:     0
    .args:
      - .actual_access:  read_only
        .address_space:  global
        .offset:         0
        .size:           8
        .value_kind:     global_buffer
      - .address_space:  global
        .offset:         8
        .size:           8
        .value_kind:     global_buffer
      - .actual_access:  read_only
        .address_space:  global
        .offset:         16
        .size:           8
        .value_kind:     global_buffer
      - .actual_access:  read_only
        .address_space:  global
        .offset:         24
        .size:           8
        .value_kind:     global_buffer
      - .actual_access:  read_only
        .address_space:  global
        .offset:         32
        .size:           8
        .value_kind:     global_buffer
      - .actual_access:  write_only
        .address_space:  global
        .offset:         40
        .size:           8
        .value_kind:     global_buffer
      - .actual_access:  read_only
        .address_space:  global
        .offset:         48
        .size:           8
        .value_kind:     global_buffer
      - .offset:         56
        .size:           4
        .value_kind:     by_value
      - .actual_access:  read_only
        .address_space:  global
        .offset:         64
        .size:           8
        .value_kind:     global_buffer
      - .actual_access:  read_only
        .address_space:  global
        .offset:         72
        .size:           8
        .value_kind:     global_buffer
      - .actual_access:  read_only
        .address_space:  global
        .offset:         80
        .size:           8
        .value_kind:     global_buffer
      - .actual_access:  read_only
        .address_space:  global
        .offset:         88
        .size:           8
        .value_kind:     global_buffer
    .group_segment_fixed_size: 147456
    .kernarg_segment_align: 8
    .kernarg_segment_size: 96
    .language:       OpenCL C
    .language_version:
      - 2
      - 0
    .max_flat_workgroup_size: 512
    .name:           _Z6conv_kILi64ELi128ELi20ELi128ELi4ELi4ELb1EEvPKDF16_S1_PKfS3_PDF16_S4_S1_fS3_S3_S3_S3_
    .private_segment_fixed_size: 0
    .sgpr_count:     43
    .sgpr_spill_count: 0
    .symbol:         _Z6conv_kILi64ELi128ELi20ELi128ELi4ELi4ELb1EEvPKDF16_S1_PKfS3_PDF16_S4_S1_fS3_S3_S3_S3_.kd
    .uniform_work_group_size: 1
    .uses_dynamic_stack: false
    .vgpr_count:     160
    .vgpr_spill_count: 0
    .wavefront_size: 64
  - .agpr_count:     0
    .args:
      - .actual_access:  read_only
        .address_space:  global
        .offset:         0
        .size:           8
        .value_kind:     global_buffer
      - .actual_access:  read_only
        .address_space:  global
        .offset:         8
        .size:           8
        .value_kind:     global_buffer
      - .actual_access:  read_only
        .address_space:  global
        .offset:         16
        .size:           8
        .value_kind:     global_buffer
      - .actual_access:  write_only
        .address_space:  global
        .offset:         24
        .size:           8
        .value_kind:     global_buffer
    .group_segment_fixed_size: 0
    .kernarg_segment_align: 8
    .kernarg_segment_size: 32
    .language:       OpenCL C
    .language_version:
      - 2
      - 0
    .max_flat_workgroup_size: 256
    .name:           _Z8finish_kILi128ELi4EEvPKDF16_PKfS3_PDF16_
    .private_segment_fixed_size: 0
    .sgpr_count:     18
    .sgpr_spill_count: 0
    .symbol:         _Z8finish_kILi128ELi4EEvPKDF16_PKfS3_PDF16_.kd
    .uniform_work_group_size: 1
    .uses_dynamic_stack: false
    .vgpr_count:     44
    .vgpr_spill_count: 0
    .wavefront_size: 64
  - .agpr_count:     0
    .args:
      - .address_space:  global
        .offset:         0
        .size:           8
        .value_kind:     global_buffer
      - .address_space:  global
        .offset:         8
        .size:           8
        .value_kind:     global_buffer
      - .address_space:  global
        .offset:         16
        .size:           8
        .value_kind:     global_buffer
      - .actual_access:  read_only
        .address_space:  global
        .offset:         24
        .size:           8
        .value_kind:     global_buffer
      - .actual_access:  write_only
        .address_space:  global
        .offset:         32
        .size:           8
        .value_kind:     global_buffer
      - .actual_access:  read_only
        .address_space:  global
        .offset:         40
        .size:           8
        .value_kind:     global_buffer
      - .address_space:  global
        .offset:         48
        .size:           8
        .value_kind:     global_buffer
      - .offset:         56
        .size:           4
        .value_kind:     by_value
      - .actual_access:  read_only
        .address_space:  global
        .offset:         64
        .size:           8
        .value_kind:     global_buffer
      - .actual_access:  read_only
        .address_space:  global
        .offset:         72
        .size:           8
        .value_kind:     global_buffer
      - .actual_access:  read_only
        .address_space:  global
        .offset:         80
        .size:           8
        .value_kind:     global_buffer
      - .actual_access:  read_only
        .address_space:  global
        .offset:         88
        .size:           8
        .value_kind:     global_buffer
    .group_segment_fixed_size: 163840
    .kernarg_segment_align: 8
    .kernarg_segment_size: 96
    .language:       OpenCL C
    .language_version:
      - 2
      - 0
    .max_flat_workgroup_size: 512
    .name:           _Z6conv_kILi128ELi256ELi3ELi64ELi1ELi1ELb0EEvPKDF16_S1_PKfS3_PDF16_S4_S1_fS3_S3_S3_S3_
    .private_segment_fixed_size: 0
    .sgpr_count:     51
    .sgpr_spill_count: 0
    .symbol:         _Z6conv_kILi128ELi256ELi3ELi64ELi1ELi1ELb0EEvPKDF16_S1_PKfS3_PDF16_S4_S1_fS3_S3_S3_S3_.kd
    .uniform_work_group_size: 1
    .uses_dynamic_stack: false
    .vgpr_count:     174
    .vgpr_spill_count: 0
    .wavefront_size: 64
  - .agpr_count:     0
    .args:
      - .address_space:  global
        .offset:         0
        .size:           8
        .value_kind:     global_buffer
      - .address_space:  global
        .offset:         8
        .size:           8
        .value_kind:     global_buffer
      - .address_space:  global
        .offset:         16
        .size:           8
        .value_kind:     global_buffer
      - .actual_access:  read_only
        .address_space:  global
        .offset:         24
        .size:           8
        .value_kind:     global_buffer
      - .actual_access:  write_only
        .address_space:  global
        .offset:         32
        .size:           8
        .value_kind:     global_buffer
      - .actual_access:  read_only
        .address_space:  global
        .offset:         40
        .size:           8
        .value_kind:     global_buffer
      - .address_space:  global
        .offset:         48
        .size:           8
        .value_kind:     global_buffer
      - .offset:         56
        .size:           4
        .value_kind:     by_value
      - .actual_access:  read_only
        .address_space:  global
        .offset:         64
        .size:           8
        .value_kind:     global_buffer
      - .actual_access:  read_only
        .address_space:  global
        .offset:         72
        .size:           8
        .value_kind:     global_buffer
      - .actual_access:  read_only
        .address_space:  global
        .offset:         80
        .size:           8
        .value_kind:     global_buffer
      - .actual_access:  read_only
        .address_space:  global
        .offset:         88
        .size:           8
        .value_kind:     global_buffer
    .group_segment_fixed_size: 163840
    .kernarg_segment_align: 8
    .kernarg_segment_size: 96
    .language:       OpenCL C
    .language_version:
      - 2
      - 0
    .max_flat_workgroup_size: 512
    .name:           _Z6conv_kILi256ELi512ELi3ELi128ELi1ELi1ELb0EEvPKDF16_S1_PKfS3_PDF16_S4_S1_fS3_S3_S3_S3_
    .private_segment_fixed_size: 0
    .sgpr_count:     64
    .sgpr_spill_count: 0
    .symbol:         _Z6conv_kILi256ELi512ELi3ELi128ELi1ELi1ELb0EEvPKDF16_S1_PKfS3_PDF16_S4_S1_fS3_S3_S3_S3_.kd
    .uniform_work_group_size: 1
    .uses_dynamic_stack: false
    .vgpr_count:     184
    .vgpr_spill_count: 0
    .wavefront_size: 64
  - .agpr_count:     0
    .args:
      - .address_space:  global
        .offset:         0
        .size:           8
        .value_kind:     global_buffer
      - .address_space:  global
        .offset:         8
        .size:           8
        .value_kind:     global_buffer
      - .address_space:  global
        .offset:         16
        .size:           8
        .value_kind:     global_buffer
      - .actual_access:  read_only
        .address_space:  global
        .offset:         24
        .size:           8
        .value_kind:     global_buffer
      - .actual_access:  write_only
        .address_space:  global
        .offset:         32
        .size:           8
        .value_kind:     global_buffer
      - .actual_access:  read_only
        .address_space:  global
        .offset:         40
        .size:           8
        .value_kind:     global_buffer
      - .address_space:  global
        .offset:         48
        .size:           8
        .value_kind:     global_buffer
      - .offset:         56
        .size:           4
        .value_kind:     by_value
      - .actual_access:  read_only
        .address_space:  global
        .offset:         64
        .size:           8
        .value_kind:     global_buffer
      - .actual_access:  read_only
        .address_space:  global
        .offset:         72
        .size:           8
        .value_kind:     global_buffer
      - .actual_access:  read_only
        .address_space:  global
        .offset:         80
        .size:           8
        .value_kind:     global_buffer
      - .actual_access:  read_only
        .address_space:  global
        .offset:         88
        .size:           8
        .value_kind:     global_buffer
    .group_segment_fixed_size: 163840
    .kernarg_segment_align: 8
    .kernarg_segment_size: 96
    .language:       OpenCL C
    .language_version:
      - 2
      - 0
    .max_flat_workgroup_size: 512
    .name:           _Z6conv_kILi512ELi256ELi3ELi64ELi1ELi1ELb0EEvPKDF16_S1_PKfS3_PDF16_S4_S1_fS3_S3_S3_S3_
    .private_segment_fixed_size: 0
    .sgpr_count:     66
    .sgpr_spill_count: 0
    .symbol:         _Z6conv_kILi512ELi256ELi3ELi64ELi1ELi1ELb0EEvPKDF16_S1_PKfS3_PDF16_S4_S1_fS3_S3_S3_S3_.kd
    .uniform_work_group_size: 1
    .uses_dynamic_stack: false
    .vgpr_count:     184
    .vgpr_spill_count: 0
    .wavefront_size: 64
  - .agpr_count:     0
    .args:
      - .address_space:  global
        .offset:         0
        .size:           8
        .value_kind:     global_buffer
      - .address_space:  global
        .offset:         8
        .size:           8
        .value_kind:     global_buffer
      - .actual_access:  read_only
        .address_space:  global
        .offset:         16
        .size:           8
        .value_kind:     global_buffer
      - .actual_access:  read_only
        .address_space:  global
        .offset:         24
        .size:           8
        .value_kind:     global_buffer
      - .actual_access:  read_only
        .address_space:  global
        .offset:         32
        .size:           8
        .value_kind:     global_buffer
      - .actual_access:  write_only
        .address_space:  global
        .offset:         40
        .size:           8
        .value_kind:     global_buffer
      - .address_space:  global
        .offset:         48
        .size:           8
        .value_kind:     global_buffer
      - .offset:         56
        .size:           4
        .value_kind:     by_value
      - .actual_access:  read_only
        .address_space:  global
        .offset:         64
        .size:           8
        .value_kind:     global_buffer
      - .actual_access:  read_only
        .address_space:  global
        .offset:         72
        .size:           8
        .value_kind:     global_buffer
      - .actual_access:  read_only
        .address_space:  global
        .offset:         80
        .size:           8
        .value_kind:     global_buffer
      - .actual_access:  read_only
        .address_space:  global
        .offset:         88
        .size:           8
        .value_kind:     global_buffer
    .group_segment_fixed_size: 163840
    .kernarg_segment_align: 8
    .kernarg_segment_size: 96
    .language:       OpenCL C
    .language_version:
      - 2
      - 0
    .max_flat_workgroup_size: 512
    .name:           _Z6conv_kILi256ELi128ELi3ELi64ELi1ELi2ELb0EEvPKDF16_S1_PKfS3_PDF16_S4_S1_fS3_S3_S3_S3_
    .private_segment_fixed_size: 0
    .sgpr_count:     55
    .sgpr_spill_count: 0
    .symbol:         _Z6conv_kILi256ELi128ELi3ELi64ELi1ELi2ELb0EEvPKDF16_S1_PKfS3_PDF16_S4_S1_fS3_S3_S3_S3_.kd
    .uniform_work_group_size: 1
    .uses_dynamic_stack: false
    .vgpr_count:     160
    .vgpr_spill_count: 0
    .wavefront_size: 64
  - .agpr_count:     0
    .args:
      - .actual_access:  read_only
        .address_space:  global
        .offset:         0
        .size:           8
        .value_kind:     global_buffer
      - .actual_access:  read_only
        .address_space:  global
        .offset:         8
        .size:           8
        .value_kind:     global_buffer
      - .actual_access:  read_only
        .address_space:  global
        .offset:         16
        .size:           8
        .value_kind:     global_buffer
      - .actual_access:  write_only
        .address_space:  global
        .offset:         24
        .size:           8
        .value_kind:     global_buffer
    .group_segment_fixed_size: 0
    .kernarg_segment_align: 8
    .kernarg_segment_size: 32
    .language:       OpenCL C
    .language_version:
      - 2
      - 0
    .max_flat_workgroup_size: 256
    .name:           _Z8finish_kILi128ELi2EEvPKDF16_PKfS3_PDF16_
    .private_segment_fixed_size: 0
    .sgpr_count:     18
    .sgpr_spill_count: 0
    .symbol:         _Z8finish_kILi128ELi2EEvPKDF16_PKfS3_PDF16_.kd
    .uniform_work_group_size: 1
    .uses_dynamic_stack: false
    .vgpr_count:     28
    .vgpr_spill_count: 0
    .wavefront_size: 64
  - .agpr_count:     0
    .args:
      - .address_space:  global
        .offset:         0
        .size:           8
        .value_kind:     global_buffer
      - .address_space:  global
        .offset:         8
        .size:           8
        .value_kind:     global_buffer
      - .actual_access:  read_only
        .address_space:  global
        .offset:         16
        .size:           8
        .value_kind:     global_buffer
      - .actual_access:  read_only
        .address_space:  global
        .offset:         24
        .size:           8
        .value_kind:     global_buffer
      - .actual_access:  read_only
        .address_space:  global
        .offset:         32
        .size:           8
        .value_kind:     global_buffer
      - .actual_access:  write_only
        .address_space:  global
        .offset:         40
        .size:           8
        .value_kind:     global_buffer
      - .address_space:  global
        .offset:         48
        .size:           8
        .value_kind:     global_buffer
      - .offset:         56
        .size:           4
        .value_kind:     by_value
      - .actual_access:  read_only
        .address_space:  global
        .offset:         64
        .size:           8
        .value_kind:     global_buffer
      - .actual_access:  read_only
        .address_space:  global
        .offset:         72
        .size:           8
        .value_kind:     global_buffer
      - .actual_access:  read_only
        .address_space:  global
        .offset:         80
        .size:           8
        .value_kind:     global_buffer
      - .actual_access:  read_only
        .address_space:  global
        .offset:         88
        .size:           8
        .value_kind:     global_buffer
    .group_segment_fixed_size: 147456
    .kernarg_segment_align: 8
    .kernarg_segment_size: 96
    .language:       OpenCL C
    .language_version:
      - 2
      - 0
    .max_flat_workgroup_size: 512
    .name:           _Z6conv_kILi128ELi64ELi20ELi64ELi4ELi4ELb0EEvPKDF16_S1_PKfS3_PDF16_S4_S1_fS3_S3_S3_S3_
    .private_segment_fixed_size: 0
    .sgpr_count:     64
    .sgpr_spill_count: 0
    .symbol:         _Z6conv_kILi128ELi64ELi20ELi64ELi4ELi4ELb0EEvPKDF16_S1_PKfS3_PDF16_S4_S1_fS3_S3_S3_S3_.kd
    .uniform_work_group_size: 1
    .uses_dynamic_stack: false
    .vgpr_count:     184
    .vgpr_spill_count: 0
    .wavefront_size: 64
